# P3 group-combine loop software-pipelined: 16 trips fully unrolled, 4 register sets of loads in flight, counted vmcnt
# baseline (speedup 1.0000x reference)
.LBB0_405:
	s_cmp_lt_i32 s64, 4
	s_cselect_b64 s[2:3], -1, 0
	s_and_b64 s[6:7], s[2:3], s[0:1]
	s_andn2_b64 vcc, exec, s[6:7]
	s_cbranch_vccnz .LBB0_497
	s_ashr_i32 s97, s96, 31
	v_mov_b32_e32 v4, v0
	s_lshl_b64 s[0:1], s[96:97], 9
	s_ashr_i32 s75, s74, 31
	v_ashrrev_i32_e32 v5, 31, v4
	v_lshl_add_u64 v[2:3], s[0:1], 0, v[4:5]
	s_mov_b64 s[0:1], 0x200000
	v_cmp_gt_u64_e32 vcc, s[0:1], v[2:3]
	s_and_saveexec_b64 s[0:1], vcc
	s_cbranch_execz .LBB0_409
	s_add_u32 s4, s62, 0x3c000000
	s_addc_u32 s5, s63, 0
	s_add_u32 s14, s62, 0x36000000
	s_addc_u32 s15, s63, 0
	s_lshl_b64 s[2:3], s[96:97], 12
	s_lshl_b64 s[8:9], s[74:75], 9
	v_lshl_add_u64 v[4:5], v[4:5], 3, s[2:3]
	s_lshl_b64 s[10:11], s[74:75], 12
	s_mov_b64 s[12:13], 0
	v_mov_b32_e32 v7, 0
	s_movk_i32 s2, 0x300
	v_mov_b64_e32 v[8:9], s[14:15]
	s_movk_i32 s3, 0x500
	v_mov_b64_e32 v[10:11], s[62:63]
	s_mov_b64 s[14:15], 0x1fffff
	s_cmp_lg_u32 s74, 0x100
	s_cbranch_scc1 .LBB0_408
	v_mov_b32_e32 v49, 0
	v_bfe_u32 v47, v2, 3, 2
	v_alignbit_b32 v50, v3, v2, 5
	v_mad_u64_u32 v[52:53], s[16:17], v50, 48, s[4:5]
	v_lshlrev_b32_e32 v48, 2, v47
	v_lshl_add_u64 v[52:53], v[52:53], 0, v[48:49]
	v_lshlrev_b32_e32 v48, 6, v47
	global_load_dword v226, v[52:53], off
	global_load_dword v227, v[52:53], off offset:16
	global_load_dword v228, v[52:53], off offset:32
	v_mad_u64_u32 v[54:55], s[16:17], v50, s2, v[8:9]
	v_and_b32_e32 v200, 56, v4
	v_mov_b32_e32 v201, v49
	v_lshl_add_u64 v[52:53], v[54:55], 0, v[48:49]
	v_lshl_add_u64 v[52:53], v[52:53], 0, v[200:201]
	global_load_dwordx2 v[194:195], v[52:53], off nt
	global_load_dwordx2 v[196:197], v[52:53], off offset:256 nt
	global_load_dwordx2 v[198:199], v[52:53], off offset:512 nt
	v_mad_u64_u32 v[56:57], s[16:17], v50, s3, v[10:11]
	v_lshl_add_u64 v[56:57], v[56:57], 0, v[48:49]
	v_lshl_add_u64 v[200:201], v[56:57], 0, v[200:201]
	v_lshl_add_u64 v[2:3], v[2:3], 0, s[8:9]
	v_lshl_add_u64 v[4:5], v[4:5], 0, s[10:11]
	v_bfe_u32 v47, v2, 3, 2
	v_alignbit_b32 v50, v3, v2, 5
	v_mad_u64_u32 v[52:53], s[16:17], v50, 48, s[4:5]
	v_lshlrev_b32_e32 v48, 2, v47
	v_lshl_add_u64 v[52:53], v[52:53], 0, v[48:49]
	v_lshlrev_b32_e32 v48, 6, v47
	global_load_dword v229, v[52:53], off
	global_load_dword v230, v[52:53], off offset:16
	global_load_dword v231, v[52:53], off offset:32
	v_mad_u64_u32 v[54:55], s[16:17], v50, s2, v[8:9]
	v_and_b32_e32 v208, 56, v4
	v_mov_b32_e32 v209, v49
	v_lshl_add_u64 v[52:53], v[54:55], 0, v[48:49]
	v_lshl_add_u64 v[52:53], v[52:53], 0, v[208:209]
	global_load_dwordx2 v[202:203], v[52:53], off nt
	global_load_dwordx2 v[204:205], v[52:53], off offset:256 nt
	global_load_dwordx2 v[206:207], v[52:53], off offset:512 nt
	v_mad_u64_u32 v[56:57], s[16:17], v50, s3, v[10:11]
	v_lshl_add_u64 v[56:57], v[56:57], 0, v[48:49]
	v_lshl_add_u64 v[208:209], v[56:57], 0, v[208:209]
	v_lshl_add_u64 v[2:3], v[2:3], 0, s[8:9]
	v_lshl_add_u64 v[4:5], v[4:5], 0, s[10:11]
	v_bfe_u32 v47, v2, 3, 2
	v_alignbit_b32 v50, v3, v2, 5
	v_mad_u64_u32 v[52:53], s[16:17], v50, 48, s[4:5]
	v_lshlrev_b32_e32 v48, 2, v47
	v_lshl_add_u64 v[52:53], v[52:53], 0, v[48:49]
	v_lshlrev_b32_e32 v48, 6, v47
	global_load_dword v232, v[52:53], off
	global_load_dword v233, v[52:53], off offset:16
	global_load_dword v234, v[52:53], off offset:32
	v_mad_u64_u32 v[54:55], s[16:17], v50, s2, v[8:9]
	v_and_b32_e32 v216, 56, v4
	v_mov_b32_e32 v217, v49
	v_lshl_add_u64 v[52:53], v[54:55], 0, v[48:49]
	v_lshl_add_u64 v[52:53], v[52:53], 0, v[216:217]
	global_load_dwordx2 v[210:211], v[52:53], off nt
	global_load_dwordx2 v[212:213], v[52:53], off offset:256 nt
	global_load_dwordx2 v[214:215], v[52:53], off offset:512 nt
	v_mad_u64_u32 v[56:57], s[16:17], v50, s3, v[10:11]
	v_lshl_add_u64 v[56:57], v[56:57], 0, v[48:49]
	v_lshl_add_u64 v[216:217], v[56:57], 0, v[216:217]
	v_lshl_add_u64 v[2:3], v[2:3], 0, s[8:9]
	v_lshl_add_u64 v[4:5], v[4:5], 0, s[10:11]
	s_waitcnt vmcnt(12)
	v_mov_b32_e32 v1, v226
	v_mov_b32_e32 v24, v227
	v_mov_b32_e32 v25, v228
	v_mov_b32_e32 v16, v194
	v_mov_b32_e32 v17, v195
	v_mov_b32_e32 v18, v196
	v_mov_b32_e32 v19, v197
	v_mov_b32_e32 v14, v198
	v_mov_b32_e32 v15, v199
	v_mov_b32_e32 v12, v200
	v_mov_b32_e32 v13, v201
	v_mov_b32_e32 v20, v7
	v_mov_b32_e32 v21, v7
	v_bfe_u32 v47, v2, 3, 2
	v_alignbit_b32 v50, v3, v2, 5
	v_mad_u64_u32 v[52:53], s[16:17], v50, 48, s[4:5]
	v_lshlrev_b32_e32 v48, 2, v47
	v_lshl_add_u64 v[52:53], v[52:53], 0, v[48:49]
	v_lshlrev_b32_e32 v48, 6, v47
	global_load_dword v235, v[52:53], off
	global_load_dword v236, v[52:53], off offset:16
	global_load_dword v237, v[52:53], off offset:32
	v_mad_u64_u32 v[54:55], s[16:17], v50, s2, v[8:9]
	v_and_b32_e32 v224, 56, v4
	v_mov_b32_e32 v225, v49
	v_lshl_add_u64 v[52:53], v[54:55], 0, v[48:49]
	v_lshl_add_u64 v[52:53], v[52:53], 0, v[224:225]
	global_load_dwordx2 v[218:219], v[52:53], off nt
	global_load_dwordx2 v[220:221], v[52:53], off offset:256 nt
	global_load_dwordx2 v[222:223], v[52:53], off offset:512 nt
	v_mad_u64_u32 v[56:57], s[16:17], v50, s3, v[10:11]
	v_lshl_add_u64 v[56:57], v[56:57], 0, v[48:49]
	v_lshl_add_u64 v[224:225], v[56:57], 0, v[224:225]
	v_lshl_add_u64 v[2:3], v[2:3], 0, s[8:9]
	v_lshl_add_u64 v[4:5], v[4:5], 0, s[10:11]
	v_max3_f32 v6, v1, v24, v25
	v_sub_f32_e32 v1, v1, v6
	v_sub_f32_e32 v22, v24, v6
	v_sub_f32_e32 v6, v25, v6
	v_exp_f32_e32 v1, v1
	v_exp_f32_e32 v40, v22
	v_exp_f32_e32 v41, v6
	v_cvt_pk_f32_fp8_e32 v[26:27], v18
	v_cvt_pk_f32_fp8_e32 v[36:37], v19
	v_add_f32_e32 v6, v1, v40
	v_add_f32_e32 v6, v41, v6
	v_div_scale_f32 v42, s[16:17], v6, v6, 1.0
	v_rcp_f32_e32 v44, v42
	v_div_scale_f32 v43, vcc, 1.0, v6, 1.0
	v_cvt_pk_f32_fp8_e32 v[22:23], v16
	v_fma_f32 v45, -v42, v44, 1.0
	v_fmac_f32_e32 v44, v45, v44
	v_mul_f32_e32 v45, v43, v44
	v_fma_f32 v46, -v42, v45, v43
	v_fmac_f32_e32 v45, v46, v44
	v_fma_f32 v42, -v42, v45, v43
	v_cvt_pk_f32_fp8_sdwa v[28:29], v18 src0_sel:WORD_1
	v_cvt_pk_f32_fp8_e32 v[34:35], v17
	v_cvt_pk_f32_fp8_sdwa v[18:19], v19 src0_sel:WORD_1
	v_div_fmas_f32 v42, v42, v44, v45
	v_cvt_pk_f32_fp8_sdwa v[24:25], v16 src0_sel:WORD_1
	v_cvt_pk_f32_fp8_e32 v[30:31], v14
	v_cvt_pk_f32_fp8_sdwa v[16:17], v17 src0_sel:WORD_1
	v_cvt_pk_f32_fp8_e32 v[38:39], v15
	v_div_fixup_f32 v42, v42, v6, 1.0
	v_mul_f32_e32 v40, v40, v42
	v_mul_f32_e32 v6, v1, v42
	v_pk_mul_f32 v[26:27], v[26:27], v[40:41] op_sel_hi:[1,0]
	v_pk_mul_f32 v[36:37], v[40:41], v[36:37] op_sel_hi:[0,1]
	v_mul_f32_e32 v42, v41, v42
	v_pk_mul_f32 v[18:19], v[40:41], v[18:19] op_sel_hi:[0,1]
	v_pk_fma_f32 v[22:23], v[22:23], v[6:7], v[26:27] op_sel_hi:[1,0,1]
	v_pk_fma_f32 v[26:27], v[6:7], v[34:35], v[36:37] op_sel_hi:[0,1,1]
	v_cvt_pk_f32_fp8_sdwa v[32:33], v14 src0_sel:WORD_1
	v_cvt_pk_f32_fp8_sdwa v[14:15], v15 src0_sel:WORD_1
	v_pk_fma_f32 v[16:17], v[6:7], v[16:17], v[18:19] op_sel_hi:[0,1,1]
	v_pk_fma_f32 v[18:19], v[30:31], v[42:43], v[22:23] op_sel_hi:[1,0,1]
	v_pk_fma_f32 v[22:23], v[42:43], v[38:39], v[26:27] op_sel_hi:[0,1,1]
	v_cvt_pk_fp8_f32 v20, v18, v19
	v_cvt_pk_fp8_f32 v21, v22, v23
	v_pk_mul_f32 v[28:29], v[28:29], v[40:41] op_sel_hi:[1,0]
	v_pk_fma_f32 v[14:15], v[42:43], v[14:15], v[16:17] op_sel_hi:[0,1,1]
	v_pk_fma_f32 v[24:25], v[24:25], v[6:7], v[28:29] op_sel_hi:[1,0,1]
	v_cvt_pk_fp8_f32 v21, v14, v15 op_sel:[0,0,1]
	v_pk_fma_f32 v[18:19], v[32:33], v[42:43], v[24:25] op_sel_hi:[1,0,1]
	v_add_co_u32_e32 v12, vcc, 0xe000000, v12
	v_cvt_pk_fp8_f32 v20, v18, v19 op_sel:[0,0,1]
	s_nop 0
	v_addc_co_u32_e32 v13, vcc, 0, v13, vcc
	global_store_dwordx2 v[12:13], v[20:21], off offset:1024
	s_waitcnt vmcnt(13)
	v_mov_b32_e32 v1, v229
	v_mov_b32_e32 v24, v230
	v_mov_b32_e32 v25, v231
	v_mov_b32_e32 v16, v202
	v_mov_b32_e32 v17, v203
	v_mov_b32_e32 v18, v204
	v_mov_b32_e32 v19, v205
	v_mov_b32_e32 v14, v206
	v_mov_b32_e32 v15, v207
	v_mov_b32_e32 v12, v208
	v_mov_b32_e32 v13, v209
	v_mov_b32_e32 v20, v7
	v_mov_b32_e32 v21, v7
	v_bfe_u32 v47, v2, 3, 2
	v_alignbit_b32 v50, v3, v2, 5
	v_mad_u64_u32 v[52:53], s[16:17], v50, 48, s[4:5]
	v_lshlrev_b32_e32 v48, 2, v47
	v_lshl_add_u64 v[52:53], v[52:53], 0, v[48:49]
	v_lshlrev_b32_e32 v48, 6, v47
	global_load_dword v226, v[52:53], off
	global_load_dword v227, v[52:53], off offset:16
	global_load_dword v228, v[52:53], off offset:32
	v_mad_u64_u32 v[54:55], s[16:17], v50, s2, v[8:9]
	v_and_b32_e32 v200, 56, v4
	v_mov_b32_e32 v201, v49
	v_lshl_add_u64 v[52:53], v[54:55], 0, v[48:49]
	v_lshl_add_u64 v[52:53], v[52:53], 0, v[200:201]
	global_load_dwordx2 v[194:195], v[52:53], off nt
	global_load_dwordx2 v[196:197], v[52:53], off offset:256 nt
	global_load_dwordx2 v[198:199], v[52:53], off offset:512 nt
	v_mad_u64_u32 v[56:57], s[16:17], v50, s3, v[10:11]
	v_lshl_add_u64 v[56:57], v[56:57], 0, v[48:49]
	v_lshl_add_u64 v[200:201], v[56:57], 0, v[200:201]
	v_lshl_add_u64 v[2:3], v[2:3], 0, s[8:9]
	v_lshl_add_u64 v[4:5], v[4:5], 0, s[10:11]
	v_max3_f32 v6, v1, v24, v25
	v_sub_f32_e32 v1, v1, v6
	v_sub_f32_e32 v22, v24, v6
	v_sub_f32_e32 v6, v25, v6
	v_exp_f32_e32 v1, v1
	v_exp_f32_e32 v40, v22
	v_exp_f32_e32 v41, v6
	v_cvt_pk_f32_fp8_e32 v[26:27], v18
	v_cvt_pk_f32_fp8_e32 v[36:37], v19
	v_add_f32_e32 v6, v1, v40
	v_add_f32_e32 v6, v41, v6
	v_div_scale_f32 v42, s[16:17], v6, v6, 1.0
	v_rcp_f32_e32 v44, v42
	v_div_scale_f32 v43, vcc, 1.0, v6, 1.0
	v_cvt_pk_f32_fp8_e32 v[22:23], v16
	v_fma_f32 v45, -v42, v44, 1.0
	v_fmac_f32_e32 v44, v45, v44
	v_mul_f32_e32 v45, v43, v44
	v_fma_f32 v46, -v42, v45, v43
	v_fmac_f32_e32 v45, v46, v44
	v_fma_f32 v42, -v42, v45, v43
	v_cvt_pk_f32_fp8_sdwa v[28:29], v18 src0_sel:WORD_1
	v_cvt_pk_f32_fp8_e32 v[34:35], v17
	v_cvt_pk_f32_fp8_sdwa v[18:19], v19 src0_sel:WORD_1
	v_div_fmas_f32 v42, v42, v44, v45
	v_cvt_pk_f32_fp8_sdwa v[24:25], v16 src0_sel:WORD_1
	v_cvt_pk_f32_fp8_e32 v[30:31], v14
	v_cvt_pk_f32_fp8_sdwa v[16:17], v17 src0_sel:WORD_1
	v_cvt_pk_f32_fp8_e32 v[38:39], v15
	v_div_fixup_f32 v42, v42, v6, 1.0
	v_mul_f32_e32 v40, v40, v42
	v_mul_f32_e32 v6, v1, v42
	v_pk_mul_f32 v[26:27], v[26:27], v[40:41] op_sel_hi:[1,0]
	v_pk_mul_f32 v[36:37], v[40:41], v[36:37] op_sel_hi:[0,1]
	v_mul_f32_e32 v42, v41, v42
	v_pk_mul_f32 v[18:19], v[40:41], v[18:19] op_sel_hi:[0,1]
	v_pk_fma_f32 v[22:23], v[22:23], v[6:7], v[26:27] op_sel_hi:[1,0,1]
	v_pk_fma_f32 v[26:27], v[6:7], v[34:35], v[36:37] op_sel_hi:[0,1,1]
	v_cvt_pk_f32_fp8_sdwa v[32:33], v14 src0_sel:WORD_1
	v_cvt_pk_f32_fp8_sdwa v[14:15], v15 src0_sel:WORD_1
	v_pk_fma_f32 v[16:17], v[6:7], v[16:17], v[18:19] op_sel_hi:[0,1,1]
	v_pk_fma_f32 v[18:19], v[30:31], v[42:43], v[22:23] op_sel_hi:[1,0,1]
	v_pk_fma_f32 v[22:23], v[42:43], v[38:39], v[26:27] op_sel_hi:[0,1,1]
	v_cvt_pk_fp8_f32 v20, v18, v19
	v_cvt_pk_fp8_f32 v21, v22, v23
	v_pk_mul_f32 v[28:29], v[28:29], v[40:41] op_sel_hi:[1,0]
	v_pk_fma_f32 v[14:15], v[42:43], v[14:15], v[16:17] op_sel_hi:[0,1,1]
	v_pk_fma_f32 v[24:25], v[24:25], v[6:7], v[28:29] op_sel_hi:[1,0,1]
	v_cvt_pk_fp8_f32 v21, v14, v15 op_sel:[0,0,1]
	v_pk_fma_f32 v[18:19], v[32:33], v[42:43], v[24:25] op_sel_hi:[1,0,1]
	v_add_co_u32_e32 v12, vcc, 0xe000000, v12
	v_cvt_pk_fp8_f32 v20, v18, v19 op_sel:[0,0,1]
	s_nop 0
	v_addc_co_u32_e32 v13, vcc, 0, v13, vcc
	global_store_dwordx2 v[12:13], v[20:21], off offset:1024
	s_waitcnt vmcnt(14)
	v_mov_b32_e32 v1, v232
	v_mov_b32_e32 v24, v233
	v_mov_b32_e32 v25, v234
	v_mov_b32_e32 v16, v210
	v_mov_b32_e32 v17, v211
	v_mov_b32_e32 v18, v212
	v_mov_b32_e32 v19, v213
	v_mov_b32_e32 v14, v214
	v_mov_b32_e32 v15, v215
	v_mov_b32_e32 v12, v216
	v_mov_b32_e32 v13, v217
	v_mov_b32_e32 v20, v7
	v_mov_b32_e32 v21, v7
	v_bfe_u32 v47, v2, 3, 2
	v_alignbit_b32 v50, v3, v2, 5
	v_mad_u64_u32 v[52:53], s[16:17], v50, 48, s[4:5]
	v_lshlrev_b32_e32 v48, 2, v47
	v_lshl_add_u64 v[52:53], v[52:53], 0, v[48:49]
	v_lshlrev_b32_e32 v48, 6, v47
	global_load_dword v229, v[52:53], off
	global_load_dword v230, v[52:53], off offset:16
	global_load_dword v231, v[52:53], off offset:32
	v_mad_u64_u32 v[54:55], s[16:17], v50, s2, v[8:9]
	v_and_b32_e32 v208, 56, v4
	v_mov_b32_e32 v209, v49
	v_lshl_add_u64 v[52:53], v[54:55], 0, v[48:49]
	v_lshl_add_u64 v[52:53], v[52:53], 0, v[208:209]
	global_load_dwordx2 v[202:203], v[52:53], off nt
	global_load_dwordx2 v[204:205], v[52:53], off offset:256 nt
	global_load_dwordx2 v[206:207], v[52:53], off offset:512 nt
	v_mad_u64_u32 v[56:57], s[16:17], v50, s3, v[10:11]
	v_lshl_add_u64 v[56:57], v[56:57], 0, v[48:49]
	v_lshl_add_u64 v[208:209], v[56:57], 0, v[208:209]
	v_lshl_add_u64 v[2:3], v[2:3], 0, s[8:9]
	v_lshl_add_u64 v[4:5], v[4:5], 0, s[10:11]
	v_max3_f32 v6, v1, v24, v25
	v_sub_f32_e32 v1, v1, v6
	v_sub_f32_e32 v22, v24, v6
	v_sub_f32_e32 v6, v25, v6
	v_exp_f32_e32 v1, v1
	v_exp_f32_e32 v40, v22
	v_exp_f32_e32 v41, v6
	v_cvt_pk_f32_fp8_e32 v[26:27], v18
	v_cvt_pk_f32_fp8_e32 v[36:37], v19
	v_add_f32_e32 v6, v1, v40
	v_add_f32_e32 v6, v41, v6
	v_div_scale_f32 v42, s[16:17], v6, v6, 1.0
	v_rcp_f32_e32 v44, v42
	v_div_scale_f32 v43, vcc, 1.0, v6, 1.0
	v_cvt_pk_f32_fp8_e32 v[22:23], v16
	v_fma_f32 v45, -v42, v44, 1.0
	v_fmac_f32_e32 v44, v45, v44
	v_mul_f32_e32 v45, v43, v44
	v_fma_f32 v46, -v42, v45, v43
	v_fmac_f32_e32 v45, v46, v44
	v_fma_f32 v42, -v42, v45, v43
	v_cvt_pk_f32_fp8_sdwa v[28:29], v18 src0_sel:WORD_1
	v_cvt_pk_f32_fp8_e32 v[34:35], v17
	v_cvt_pk_f32_fp8_sdwa v[18:19], v19 src0_sel:WORD_1
	v_div_fmas_f32 v42, v42, v44, v45
	v_cvt_pk_f32_fp8_sdwa v[24:25], v16 src0_sel:WORD_1
	v_cvt_pk_f32_fp8_e32 v[30:31], v14
	v_cvt_pk_f32_fp8_sdwa v[16:17], v17 src0_sel:WORD_1
	v_cvt_pk_f32_fp8_e32 v[38:39], v15
	v_div_fixup_f32 v42, v42, v6, 1.0
	v_mul_f32_e32 v40, v40, v42
	v_mul_f32_e32 v6, v1, v42
	v_pk_mul_f32 v[26:27], v[26:27], v[40:41] op_sel_hi:[1,0]
	v_pk_mul_f32 v[36:37], v[40:41], v[36:37] op_sel_hi:[0,1]
	v_mul_f32_e32 v42, v41, v42
	v_pk_mul_f32 v[18:19], v[40:41], v[18:19] op_sel_hi:[0,1]
	v_pk_fma_f32 v[22:23], v[22:23], v[6:7], v[26:27] op_sel_hi:[1,0,1]
	v_pk_fma_f32 v[26:27], v[6:7], v[34:35], v[36:37] op_sel_hi:[0,1,1]
	v_cvt_pk_f32_fp8_sdwa v[32:33], v14 src0_sel:WORD_1
	v_cvt_pk_f32_fp8_sdwa v[14:15], v15 src0_sel:WORD_1
	v_pk_fma_f32 v[16:17], v[6:7], v[16:17], v[18:19] op_sel_hi:[0,1,1]
	v_pk_fma_f32 v[18:19], v[30:31], v[42:43], v[22:23] op_sel_hi:[1,0,1]
	v_pk_fma_f32 v[22:23], v[42:43], v[38:39], v[26:27] op_sel_hi:[0,1,1]
	v_cvt_pk_fp8_f32 v20, v18, v19
	v_cvt_pk_fp8_f32 v21, v22, v23
	v_pk_mul_f32 v[28:29], v[28:29], v[40:41] op_sel_hi:[1,0]
	v_pk_fma_f32 v[14:15], v[42:43], v[14:15], v[16:17] op_sel_hi:[0,1,1]
	v_pk_fma_f32 v[24:25], v[24:25], v[6:7], v[28:29] op_sel_hi:[1,0,1]
	v_cvt_pk_fp8_f32 v21, v14, v15 op_sel:[0,0,1]
	v_pk_fma_f32 v[18:19], v[32:33], v[42:43], v[24:25] op_sel_hi:[1,0,1]
	v_add_co_u32_e32 v12, vcc, 0xe000000, v12
	v_cvt_pk_fp8_f32 v20, v18, v19 op_sel:[0,0,1]
	s_nop 0
	v_addc_co_u32_e32 v13, vcc, 0, v13, vcc
	global_store_dwordx2 v[12:13], v[20:21], off offset:1024
	s_waitcnt vmcnt(15)
	v_mov_b32_e32 v1, v235
	v_mov_b32_e32 v24, v236
	v_mov_b32_e32 v25, v237
	v_mov_b32_e32 v16, v218
	v_mov_b32_e32 v17, v219
	v_mov_b32_e32 v18, v220
	v_mov_b32_e32 v19, v221
	v_mov_b32_e32 v14, v222
	v_mov_b32_e32 v15, v223
	v_mov_b32_e32 v12, v224
	v_mov_b32_e32 v13, v225
	v_mov_b32_e32 v20, v7
	v_mov_b32_e32 v21, v7
	v_bfe_u32 v47, v2, 3, 2
	v_alignbit_b32 v50, v3, v2, 5
	v_mad_u64_u32 v[52:53], s[16:17], v50, 48, s[4:5]
	v_lshlrev_b32_e32 v48, 2, v47
	v_lshl_add_u64 v[52:53], v[52:53], 0, v[48:49]
	v_lshlrev_b32_e32 v48, 6, v47
	global_load_dword v232, v[52:53], off
	global_load_dword v233, v[52:53], off offset:16
	global_load_dword v234, v[52:53], off offset:32
	v_mad_u64_u32 v[54:55], s[16:17], v50, s2, v[8:9]
	v_and_b32_e32 v216, 56, v4
	v_mov_b32_e32 v217, v49
	v_lshl_add_u64 v[52:53], v[54:55], 0, v[48:49]
	v_lshl_add_u64 v[52:53], v[52:53], 0, v[216:217]
	global_load_dwordx2 v[210:211], v[52:53], off nt
	global_load_dwordx2 v[212:213], v[52:53], off offset:256 nt
	global_load_dwordx2 v[214:215], v[52:53], off offset:512 nt
	v_mad_u64_u32 v[56:57], s[16:17], v50, s3, v[10:11]
	v_lshl_add_u64 v[56:57], v[56:57], 0, v[48:49]
	v_lshl_add_u64 v[216:217], v[56:57], 0, v[216:217]
	v_lshl_add_u64 v[2:3], v[2:3], 0, s[8:9]
	v_lshl_add_u64 v[4:5], v[4:5], 0, s[10:11]
	v_max3_f32 v6, v1, v24, v25
	v_sub_f32_e32 v1, v1, v6
	v_sub_f32_e32 v22, v24, v6
	v_sub_f32_e32 v6, v25, v6
	v_exp_f32_e32 v1, v1
	v_exp_f32_e32 v40, v22
	v_exp_f32_e32 v41, v6
	v_cvt_pk_f32_fp8_e32 v[26:27], v18
	v_cvt_pk_f32_fp8_e32 v[36:37], v19
	v_add_f32_e32 v6, v1, v40
	v_add_f32_e32 v6, v41, v6
	v_div_scale_f32 v42, s[16:17], v6, v6, 1.0
	v_rcp_f32_e32 v44, v42
	v_div_scale_f32 v43, vcc, 1.0, v6, 1.0
	v_cvt_pk_f32_fp8_e32 v[22:23], v16
	v_fma_f32 v45, -v42, v44, 1.0
	v_fmac_f32_e32 v44, v45, v44
	v_mul_f32_e32 v45, v43, v44
	v_fma_f32 v46, -v42, v45, v43
	v_fmac_f32_e32 v45, v46, v44
	v_fma_f32 v42, -v42, v45, v43
	v_cvt_pk_f32_fp8_sdwa v[28:29], v18 src0_sel:WORD_1
	v_cvt_pk_f32_fp8_e32 v[34:35], v17
	v_cvt_pk_f32_fp8_sdwa v[18:19], v19 src0_sel:WORD_1
	v_div_fmas_f32 v42, v42, v44, v45
	v_cvt_pk_f32_fp8_sdwa v[24:25], v16 src0_sel:WORD_1
	v_cvt_pk_f32_fp8_e32 v[30:31], v14
	v_cvt_pk_f32_fp8_sdwa v[16:17], v17 src0_sel:WORD_1
	v_cvt_pk_f32_fp8_e32 v[38:39], v15
	v_div_fixup_f32 v42, v42, v6, 1.0
	v_mul_f32_e32 v40, v40, v42
	v_mul_f32_e32 v6, v1, v42
	v_pk_mul_f32 v[26:27], v[26:27], v[40:41] op_sel_hi:[1,0]
	v_pk_mul_f32 v[36:37], v[40:41], v[36:37] op_sel_hi:[0,1]
	v_mul_f32_e32 v42, v41, v42
	v_pk_mul_f32 v[18:19], v[40:41], v[18:19] op_sel_hi:[0,1]
	v_pk_fma_f32 v[22:23], v[22:23], v[6:7], v[26:27] op_sel_hi:[1,0,1]
	v_pk_fma_f32 v[26:27], v[6:7], v[34:35], v[36:37] op_sel_hi:[0,1,1]
	v_cvt_pk_f32_fp8_sdwa v[32:33], v14 src0_sel:WORD_1
	v_cvt_pk_f32_fp8_sdwa v[14:15], v15 src0_sel:WORD_1
	v_pk_fma_f32 v[16:17], v[6:7], v[16:17], v[18:19] op_sel_hi:[0,1,1]
	v_pk_fma_f32 v[18:19], v[30:31], v[42:43], v[22:23] op_sel_hi:[1,0,1]
	v_pk_fma_f32 v[22:23], v[42:43], v[38:39], v[26:27] op_sel_hi:[0,1,1]
	v_cvt_pk_fp8_f32 v20, v18, v19
	v_cvt_pk_fp8_f32 v21, v22, v23
	v_pk_mul_f32 v[28:29], v[28:29], v[40:41] op_sel_hi:[1,0]
	v_pk_fma_f32 v[14:15], v[42:43], v[14:15], v[16:17] op_sel_hi:[0,1,1]
	v_pk_fma_f32 v[24:25], v[24:25], v[6:7], v[28:29] op_sel_hi:[1,0,1]
	v_cvt_pk_fp8_f32 v21, v14, v15 op_sel:[0,0,1]
	v_pk_fma_f32 v[18:19], v[32:33], v[42:43], v[24:25] op_sel_hi:[1,0,1]
	v_add_co_u32_e32 v12, vcc, 0xe000000, v12
	v_cvt_pk_fp8_f32 v20, v18, v19 op_sel:[0,0,1]
	s_nop 0
	v_addc_co_u32_e32 v13, vcc, 0, v13, vcc
	global_store_dwordx2 v[12:13], v[20:21], off offset:1024
	s_waitcnt vmcnt(15)
	v_mov_b32_e32 v1, v226
	v_mov_b32_e32 v24, v227
	v_mov_b32_e32 v25, v228
	v_mov_b32_e32 v16, v194
	v_mov_b32_e32 v17, v195
	v_mov_b32_e32 v18, v196
	v_mov_b32_e32 v19, v197
	v_mov_b32_e32 v14, v198
	v_mov_b32_e32 v15, v199
	v_mov_b32_e32 v12, v200
	v_mov_b32_e32 v13, v201
	v_mov_b32_e32 v20, v7
	v_mov_b32_e32 v21, v7
	v_bfe_u32 v47, v2, 3, 2
	v_alignbit_b32 v50, v3, v2, 5
	v_mad_u64_u32 v[52:53], s[16:17], v50, 48, s[4:5]
	v_lshlrev_b32_e32 v48, 2, v47
	v_lshl_add_u64 v[52:53], v[52:53], 0, v[48:49]
	v_lshlrev_b32_e32 v48, 6, v47
	global_load_dword v235, v[52:53], off
	global_load_dword v236, v[52:53], off offset:16
	global_load_dword v237, v[52:53], off offset:32
	v_mad_u64_u32 v[54:55], s[16:17], v50, s2, v[8:9]
	v_and_b32_e32 v224, 56, v4
	v_mov_b32_e32 v225, v49
	v_lshl_add_u64 v[52:53], v[54:55], 0, v[48:49]
	v_lshl_add_u64 v[52:53], v[52:53], 0, v[224:225]
	global_load_dwordx2 v[218:219], v[52:53], off nt
	global_load_dwordx2 v[220:221], v[52:53], off offset:256 nt
	global_load_dwordx2 v[222:223], v[52:53], off offset:512 nt
	v_mad_u64_u32 v[56:57], s[16:17], v50, s3, v[10:11]
	v_lshl_add_u64 v[56:57], v[56:57], 0, v[48:49]
	v_lshl_add_u64 v[224:225], v[56:57], 0, v[224:225]
	v_lshl_add_u64 v[2:3], v[2:3], 0, s[8:9]
	v_lshl_add_u64 v[4:5], v[4:5], 0, s[10:11]
	v_max3_f32 v6, v1, v24, v25
	v_sub_f32_e32 v1, v1, v6
	v_sub_f32_e32 v22, v24, v6
	v_sub_f32_e32 v6, v25, v6
	v_exp_f32_e32 v1, v1
	v_exp_f32_e32 v40, v22
	v_exp_f32_e32 v41, v6
	v_cvt_pk_f32_fp8_e32 v[26:27], v18
	v_cvt_pk_f32_fp8_e32 v[36:37], v19
	v_add_f32_e32 v6, v1, v40
	v_add_f32_e32 v6, v41, v6
	v_div_scale_f32 v42, s[16:17], v6, v6, 1.0
	v_rcp_f32_e32 v44, v42
	v_div_scale_f32 v43, vcc, 1.0, v6, 1.0
	v_cvt_pk_f32_fp8_e32 v[22:23], v16
	v_fma_f32 v45, -v42, v44, 1.0
	v_fmac_f32_e32 v44, v45, v44
	v_mul_f32_e32 v45, v43, v44
	v_fma_f32 v46, -v42, v45, v43
	v_fmac_f32_e32 v45, v46, v44
	v_fma_f32 v42, -v42, v45, v43
	v_cvt_pk_f32_fp8_sdwa v[28:29], v18 src0_sel:WORD_1
	v_cvt_pk_f32_fp8_e32 v[34:35], v17
	v_cvt_pk_f32_fp8_sdwa v[18:19], v19 src0_sel:WORD_1
	v_div_fmas_f32 v42, v42, v44, v45
	v_cvt_pk_f32_fp8_sdwa v[24:25], v16 src0_sel:WORD_1
	v_cvt_pk_f32_fp8_e32 v[30:31], v14
	v_cvt_pk_f32_fp8_sdwa v[16:17], v17 src0_sel:WORD_1
	v_cvt_pk_f32_fp8_e32 v[38:39], v15
	v_div_fixup_f32 v42, v42, v6, 1.0
	v_mul_f32_e32 v40, v40, v42
	v_mul_f32_e32 v6, v1, v42
	v_pk_mul_f32 v[26:27], v[26:27], v[40:41] op_sel_hi:[1,0]
	v_pk_mul_f32 v[36:37], v[40:41], v[36:37] op_sel_hi:[0,1]
	v_mul_f32_e32 v42, v41, v42
	v_pk_mul_f32 v[18:19], v[40:41], v[18:19] op_sel_hi:[0,1]
	v_pk_fma_f32 v[22:23], v[22:23], v[6:7], v[26:27] op_sel_hi:[1,0,1]
	v_pk_fma_f32 v[26:27], v[6:7], v[34:35], v[36:37] op_sel_hi:[0,1,1]
	v_cvt_pk_f32_fp8_sdwa v[32:33], v14 src0_sel:WORD_1
	v_cvt_pk_f32_fp8_sdwa v[14:15], v15 src0_sel:WORD_1
	v_pk_fma_f32 v[16:17], v[6:7], v[16:17], v[18:19] op_sel_hi:[0,1,1]
	v_pk_fma_f32 v[18:19], v[30:31], v[42:43], v[22:23] op_sel_hi:[1,0,1]
	v_pk_fma_f32 v[22:23], v[42:43], v[38:39], v[26:27] op_sel_hi:[0,1,1]
	v_cvt_pk_fp8_f32 v20, v18, v19
	v_cvt_pk_fp8_f32 v21, v22, v23
	v_pk_mul_f32 v[28:29], v[28:29], v[40:41] op_sel_hi:[1,0]
	v_pk_fma_f32 v[14:15], v[42:43], v[14:15], v[16:17] op_sel_hi:[0,1,1]
	v_pk_fma_f32 v[24:25], v[24:25], v[6:7], v[28:29] op_sel_hi:[1,0,1]
	v_cvt_pk_fp8_f32 v21, v14, v15 op_sel:[0,0,1]
	v_pk_fma_f32 v[18:19], v[32:33], v[42:43], v[24:25] op_sel_hi:[1,0,1]
	v_add_co_u32_e32 v12, vcc, 0xe000000, v12
	v_cvt_pk_fp8_f32 v20, v18, v19 op_sel:[0,0,1]
	s_nop 0
	v_addc_co_u32_e32 v13, vcc, 0, v13, vcc
	global_store_dwordx2 v[12:13], v[20:21], off offset:1024
	s_waitcnt vmcnt(15)
	v_mov_b32_e32 v1, v229
	v_mov_b32_e32 v24, v230
	v_mov_b32_e32 v25, v231
	v_mov_b32_e32 v16, v202
	v_mov_b32_e32 v17, v203
	v_mov_b32_e32 v18, v204
	v_mov_b32_e32 v19, v205
	v_mov_b32_e32 v14, v206
	v_mov_b32_e32 v15, v207
	v_mov_b32_e32 v12, v208
	v_mov_b32_e32 v13, v209
	v_mov_b32_e32 v20, v7
	v_mov_b32_e32 v21, v7
	v_bfe_u32 v47, v2, 3, 2
	v_alignbit_b32 v50, v3, v2, 5
	v_mad_u64_u32 v[52:53], s[16:17], v50, 48, s[4:5]
	v_lshlrev_b32_e32 v48, 2, v47
	v_lshl_add_u64 v[52:53], v[52:53], 0, v[48:49]
	v_lshlrev_b32_e32 v48, 6, v47
	global_load_dword v226, v[52:53], off
	global_load_dword v227, v[52:53], off offset:16
	global_load_dword v228, v[52:53], off offset:32
	v_mad_u64_u32 v[54:55], s[16:17], v50, s2, v[8:9]
	v_and_b32_e32 v200, 56, v4
	v_mov_b32_e32 v201, v49
	v_lshl_add_u64 v[52:53], v[54:55], 0, v[48:49]
	v_lshl_add_u64 v[52:53], v[52:53], 0, v[200:201]
	global_load_dwordx2 v[194:195], v[52:53], off nt
	global_load_dwordx2 v[196:197], v[52:53], off offset:256 nt
	global_load_dwordx2 v[198:199], v[52:53], off offset:512 nt
	v_mad_u64_u32 v[56:57], s[16:17], v50, s3, v[10:11]
	v_lshl_add_u64 v[56:57], v[56:57], 0, v[48:49]
	v_lshl_add_u64 v[200:201], v[56:57], 0, v[200:201]
	v_lshl_add_u64 v[2:3], v[2:3], 0, s[8:9]
	v_lshl_add_u64 v[4:5], v[4:5], 0, s[10:11]
	v_max3_f32 v6, v1, v24, v25
	v_sub_f32_e32 v1, v1, v6
	v_sub_f32_e32 v22, v24, v6
	v_sub_f32_e32 v6, v25, v6
	v_exp_f32_e32 v1, v1
	v_exp_f32_e32 v40, v22
	v_exp_f32_e32 v41, v6
	v_cvt_pk_f32_fp8_e32 v[26:27], v18
	v_cvt_pk_f32_fp8_e32 v[36:37], v19
	v_add_f32_e32 v6, v1, v40
	v_add_f32_e32 v6, v41, v6
	v_div_scale_f32 v42, s[16:17], v6, v6, 1.0
	v_rcp_f32_e32 v44, v42
	v_div_scale_f32 v43, vcc, 1.0, v6, 1.0
	v_cvt_pk_f32_fp8_e32 v[22:23], v16
	v_fma_f32 v45, -v42, v44, 1.0
	v_fmac_f32_e32 v44, v45, v44
	v_mul_f32_e32 v45, v43, v44
	v_fma_f32 v46, -v42, v45, v43
	v_fmac_f32_e32 v45, v46, v44
	v_fma_f32 v42, -v42, v45, v43
	v_cvt_pk_f32_fp8_sdwa v[28:29], v18 src0_sel:WORD_1
	v_cvt_pk_f32_fp8_e32 v[34:35], v17
	v_cvt_pk_f32_fp8_sdwa v[18:19], v19 src0_sel:WORD_1
	v_div_fmas_f32 v42, v42, v44, v45
	v_cvt_pk_f32_fp8_sdwa v[24:25], v16 src0_sel:WORD_1
	v_cvt_pk_f32_fp8_e32 v[30:31], v14
	v_cvt_pk_f32_fp8_sdwa v[16:17], v17 src0_sel:WORD_1
	v_cvt_pk_f32_fp8_e32 v[38:39], v15
	v_div_fixup_f32 v42, v42, v6, 1.0
	v_mul_f32_e32 v40, v40, v42
	v_mul_f32_e32 v6, v1, v42
	v_pk_mul_f32 v[26:27], v[26:27], v[40:41] op_sel_hi:[1,0]
	v_pk_mul_f32 v[36:37], v[40:41], v[36:37] op_sel_hi:[0,1]
	v_mul_f32_e32 v42, v41, v42
	v_pk_mul_f32 v[18:19], v[40:41], v[18:19] op_sel_hi:[0,1]
	v_pk_fma_f32 v[22:23], v[22:23], v[6:7], v[26:27] op_sel_hi:[1,0,1]
	v_pk_fma_f32 v[26:27], v[6:7], v[34:35], v[36:37] op_sel_hi:[0,1,1]
	v_cvt_pk_f32_fp8_sdwa v[32:33], v14 src0_sel:WORD_1
	v_cvt_pk_f32_fp8_sdwa v[14:15], v15 src0_sel:WORD_1
	v_pk_fma_f32 v[16:17], v[6:7], v[16:17], v[18:19] op_sel_hi:[0,1,1]
	v_pk_fma_f32 v[18:19], v[30:31], v[42:43], v[22:23] op_sel_hi:[1,0,1]
	v_pk_fma_f32 v[22:23], v[42:43], v[38:39], v[26:27] op_sel_hi:[0,1,1]
	v_cvt_pk_fp8_f32 v20, v18, v19
	v_cvt_pk_fp8_f32 v21, v22, v23
	v_pk_mul_f32 v[28:29], v[28:29], v[40:41] op_sel_hi:[1,0]
	v_pk_fma_f32 v[14:15], v[42:43], v[14:15], v[16:17] op_sel_hi:[0,1,1]
	v_pk_fma_f32 v[24:25], v[24:25], v[6:7], v[28:29] op_sel_hi:[1,0,1]
	v_cvt_pk_fp8_f32 v21, v14, v15 op_sel:[0,0,1]
	v_pk_fma_f32 v[18:19], v[32:33], v[42:43], v[24:25] op_sel_hi:[1,0,1]
	v_add_co_u32_e32 v12, vcc, 0xe000000, v12
	v_cvt_pk_fp8_f32 v20, v18, v19 op_sel:[0,0,1]
	s_nop 0
	v_addc_co_u32_e32 v13, vcc, 0, v13, vcc
	global_store_dwordx2 v[12:13], v[20:21], off offset:1024
	s_waitcnt vmcnt(15)
	v_mov_b32_e32 v1, v232
	v_mov_b32_e32 v24, v233
	v_mov_b32_e32 v25, v234
	v_mov_b32_e32 v16, v210
	v_mov_b32_e32 v17, v211
	v_mov_b32_e32 v18, v212
	v_mov_b32_e32 v19, v213
	v_mov_b32_e32 v14, v214
	v_mov_b32_e32 v15, v215
	v_mov_b32_e32 v12, v216
	v_mov_b32_e32 v13, v217
	v_mov_b32_e32 v20, v7
	v_mov_b32_e32 v21, v7
	v_bfe_u32 v47, v2, 3, 2
	v_alignbit_b32 v50, v3, v2, 5
	v_mad_u64_u32 v[52:53], s[16:17], v50, 48, s[4:5]
	v_lshlrev_b32_e32 v48, 2, v47
	v_lshl_add_u64 v[52:53], v[52:53], 0, v[48:49]
	v_lshlrev_b32_e32 v48, 6, v47
	global_load_dword v229, v[52:53], off
	global_load_dword v230, v[52:53], off offset:16
	global_load_dword v231, v[52:53], off offset:32
	v_mad_u64_u32 v[54:55], s[16:17], v50, s2, v[8:9]
	v_and_b32_e32 v208, 56, v4
	v_mov_b32_e32 v209, v49
	v_lshl_add_u64 v[52:53], v[54:55], 0, v[48:49]
	v_lshl_add_u64 v[52:53], v[52:53], 0, v[208:209]
	global_load_dwordx2 v[202:203], v[52:53], off nt
	global_load_dwordx2 v[204:205], v[52:53], off offset:256 nt
	global_load_dwordx2 v[206:207], v[52:53], off offset:512 nt
	v_mad_u64_u32 v[56:57], s[16:17], v50, s3, v[10:11]
	v_lshl_add_u64 v[56:57], v[56:57], 0, v[48:49]
	v_lshl_add_u64 v[208:209], v[56:57], 0, v[208:209]
	v_lshl_add_u64 v[2:3], v[2:3], 0, s[8:9]
	v_lshl_add_u64 v[4:5], v[4:5], 0, s[10:11]
	v_max3_f32 v6, v1, v24, v25
	v_sub_f32_e32 v1, v1, v6
	v_sub_f32_e32 v22, v24, v6
	v_sub_f32_e32 v6, v25, v6
	v_exp_f32_e32 v1, v1
	v_exp_f32_e32 v40, v22
	v_exp_f32_e32 v41, v6
	v_cvt_pk_f32_fp8_e32 v[26:27], v18
	v_cvt_pk_f32_fp8_e32 v[36:37], v19
	v_add_f32_e32 v6, v1, v40
	v_add_f32_e32 v6, v41, v6
	v_div_scale_f32 v42, s[16:17], v6, v6, 1.0
	v_rcp_f32_e32 v44, v42
	v_div_scale_f32 v43, vcc, 1.0, v6, 1.0
	v_cvt_pk_f32_fp8_e32 v[22:23], v16
	v_fma_f32 v45, -v42, v44, 1.0
	v_fmac_f32_e32 v44, v45, v44
	v_mul_f32_e32 v45, v43, v44
	v_fma_f32 v46, -v42, v45, v43
	v_fmac_f32_e32 v45, v46, v44
	v_fma_f32 v42, -v42, v45, v43
	v_cvt_pk_f32_fp8_sdwa v[28:29], v18 src0_sel:WORD_1
	v_cvt_pk_f32_fp8_e32 v[34:35], v17
	v_cvt_pk_f32_fp8_sdwa v[18:19], v19 src0_sel:WORD_1
	v_div_fmas_f32 v42, v42, v44, v45
	v_cvt_pk_f32_fp8_sdwa v[24:25], v16 src0_sel:WORD_1
	v_cvt_pk_f32_fp8_e32 v[30:31], v14
	v_cvt_pk_f32_fp8_sdwa v[16:17], v17 src0_sel:WORD_1
	v_cvt_pk_f32_fp8_e32 v[38:39], v15
	v_div_fixup_f32 v42, v42, v6, 1.0
	v_mul_f32_e32 v40, v40, v42
	v_mul_f32_e32 v6, v1, v42
	v_pk_mul_f32 v[26:27], v[26:27], v[40:41] op_sel_hi:[1,0]
	v_pk_mul_f32 v[36:37], v[40:41], v[36:37] op_sel_hi:[0,1]
	v_mul_f32_e32 v42, v41, v42
	v_pk_mul_f32 v[18:19], v[40:41], v[18:19] op_sel_hi:[0,1]
	v_pk_fma_f32 v[22:23], v[22:23], v[6:7], v[26:27] op_sel_hi:[1,0,1]
	v_pk_fma_f32 v[26:27], v[6:7], v[34:35], v[36:37] op_sel_hi:[0,1,1]
	v_cvt_pk_f32_fp8_sdwa v[32:33], v14 src0_sel:WORD_1
	v_cvt_pk_f32_fp8_sdwa v[14:15], v15 src0_sel:WORD_1
	v_pk_fma_f32 v[16:17], v[6:7], v[16:17], v[18:19] op_sel_hi:[0,1,1]
	v_pk_fma_f32 v[18:19], v[30:31], v[42:43], v[22:23] op_sel_hi:[1,0,1]
	v_pk_fma_f32 v[22:23], v[42:43], v[38:39], v[26:27] op_sel_hi:[0,1,1]
	v_cvt_pk_fp8_f32 v20, v18, v19
	v_cvt_pk_fp8_f32 v21, v22, v23
	v_pk_mul_f32 v[28:29], v[28:29], v[40:41] op_sel_hi:[1,0]
	v_pk_fma_f32 v[14:15], v[42:43], v[14:15], v[16:17] op_sel_hi:[0,1,1]
	v_pk_fma_f32 v[24:25], v[24:25], v[6:7], v[28:29] op_sel_hi:[1,0,1]
	v_cvt_pk_fp8_f32 v21, v14, v15 op_sel:[0,0,1]
	v_pk_fma_f32 v[18:19], v[32:33], v[42:43], v[24:25] op_sel_hi:[1,0,1]
	v_add_co_u32_e32 v12, vcc, 0xe000000, v12
	v_cvt_pk_fp8_f32 v20, v18, v19 op_sel:[0,0,1]
	s_nop 0
	v_addc_co_u32_e32 v13, vcc, 0, v13, vcc
	global_store_dwordx2 v[12:13], v[20:21], off offset:1024
	s_waitcnt vmcnt(15)
	v_mov_b32_e32 v1, v235
	v_mov_b32_e32 v24, v236
	v_mov_b32_e32 v25, v237
	v_mov_b32_e32 v16, v218
	v_mov_b32_e32 v17, v219
	v_mov_b32_e32 v18, v220
	v_mov_b32_e32 v19, v221
	v_mov_b32_e32 v14, v222
	v_mov_b32_e32 v15, v223
	v_mov_b32_e32 v12, v224
	v_mov_b32_e32 v13, v225
	v_mov_b32_e32 v20, v7
	v_mov_b32_e32 v21, v7
	v_bfe_u32 v47, v2, 3, 2
	v_alignbit_b32 v50, v3, v2, 5
	v_mad_u64_u32 v[52:53], s[16:17], v50, 48, s[4:5]
	v_lshlrev_b32_e32 v48, 2, v47
	v_lshl_add_u64 v[52:53], v[52:53], 0, v[48:49]
	v_lshlrev_b32_e32 v48, 6, v47
	global_load_dword v232, v[52:53], off
	global_load_dword v233, v[52:53], off offset:16
	global_load_dword v234, v[52:53], off offset:32
	v_mad_u64_u32 v[54:55], s[16:17], v50, s2, v[8:9]
	v_and_b32_e32 v216, 56, v4
	v_mov_b32_e32 v217, v49
	v_lshl_add_u64 v[52:53], v[54:55], 0, v[48:49]
	v_lshl_add_u64 v[52:53], v[52:53], 0, v[216:217]
	global_load_dwordx2 v[210:211], v[52:53], off nt
	global_load_dwordx2 v[212:213], v[52:53], off offset:256 nt
	global_load_dwordx2 v[214:215], v[52:53], off offset:512 nt
	v_mad_u64_u32 v[56:57], s[16:17], v50, s3, v[10:11]
	v_lshl_add_u64 v[56:57], v[56:57], 0, v[48:49]
	v_lshl_add_u64 v[216:217], v[56:57], 0, v[216:217]
	v_lshl_add_u64 v[2:3], v[2:3], 0, s[8:9]
	v_lshl_add_u64 v[4:5], v[4:5], 0, s[10:11]
	v_max3_f32 v6, v1, v24, v25
	v_sub_f32_e32 v1, v1, v6
	v_sub_f32_e32 v22, v24, v6
	v_sub_f32_e32 v6, v25, v6
	v_exp_f32_e32 v1, v1
	v_exp_f32_e32 v40, v22
	v_exp_f32_e32 v41, v6
	v_cvt_pk_f32_fp8_e32 v[26:27], v18
	v_cvt_pk_f32_fp8_e32 v[36:37], v19
	v_add_f32_e32 v6, v1, v40
	v_add_f32_e32 v6, v41, v6
	v_div_scale_f32 v42, s[16:17], v6, v6, 1.0
	v_rcp_f32_e32 v44, v42
	v_div_scale_f32 v43, vcc, 1.0, v6, 1.0
	v_cvt_pk_f32_fp8_e32 v[22:23], v16
	v_fma_f32 v45, -v42, v44, 1.0
	v_fmac_f32_e32 v44, v45, v44
	v_mul_f32_e32 v45, v43, v44
	v_fma_f32 v46, -v42, v45, v43
	v_fmac_f32_e32 v45, v46, v44
	v_fma_f32 v42, -v42, v45, v43
	v_cvt_pk_f32_fp8_sdwa v[28:29], v18 src0_sel:WORD_1
	v_cvt_pk_f32_fp8_e32 v[34:35], v17
	v_cvt_pk_f32_fp8_sdwa v[18:19], v19 src0_sel:WORD_1
	v_div_fmas_f32 v42, v42, v44, v45
	v_cvt_pk_f32_fp8_sdwa v[24:25], v16 src0_sel:WORD_1
	v_cvt_pk_f32_fp8_e32 v[30:31], v14
	v_cvt_pk_f32_fp8_sdwa v[16:17], v17 src0_sel:WORD_1
	v_cvt_pk_f32_fp8_e32 v[38:39], v15
	v_div_fixup_f32 v42, v42, v6, 1.0
	v_mul_f32_e32 v40, v40, v42
	v_mul_f32_e32 v6, v1, v42
	v_pk_mul_f32 v[26:27], v[26:27], v[40:41] op_sel_hi:[1,0]
	v_pk_mul_f32 v[36:37], v[40:41], v[36:37] op_sel_hi:[0,1]
	v_mul_f32_e32 v42, v41, v42
	v_pk_mul_f32 v[18:19], v[40:41], v[18:19] op_sel_hi:[0,1]
	v_pk_fma_f32 v[22:23], v[22:23], v[6:7], v[26:27] op_sel_hi:[1,0,1]
	v_pk_fma_f32 v[26:27], v[6:7], v[34:35], v[36:37] op_sel_hi:[0,1,1]
	v_cvt_pk_f32_fp8_sdwa v[32:33], v14 src0_sel:WORD_1
	v_cvt_pk_f32_fp8_sdwa v[14:15], v15 src0_sel:WORD_1
	v_pk_fma_f32 v[16:17], v[6:7], v[16:17], v[18:19] op_sel_hi:[0,1,1]
	v_pk_fma_f32 v[18:19], v[30:31], v[42:43], v[22:23] op_sel_hi:[1,0,1]
	v_pk_fma_f32 v[22:23], v[42:43], v[38:39], v[26:27] op_sel_hi:[0,1,1]
	v_cvt_pk_fp8_f32 v20, v18, v19
	v_cvt_pk_fp8_f32 v21, v22, v23
	v_pk_mul_f32 v[28:29], v[28:29], v[40:41] op_sel_hi:[1,0]
	v_pk_fma_f32 v[14:15], v[42:43], v[14:15], v[16:17] op_sel_hi:[0,1,1]
	v_pk_fma_f32 v[24:25], v[24:25], v[6:7], v[28:29] op_sel_hi:[1,0,1]
	v_cvt_pk_fp8_f32 v21, v14, v15 op_sel:[0,0,1]
	v_pk_fma_f32 v[18:19], v[32:33], v[42:43], v[24:25] op_sel_hi:[1,0,1]
	v_add_co_u32_e32 v12, vcc, 0xe000000, v12
	v_cvt_pk_fp8_f32 v20, v18, v19 op_sel:[0,0,1]
	s_nop 0
	v_addc_co_u32_e32 v13, vcc, 0, v13, vcc
	global_store_dwordx2 v[12:13], v[20:21], off offset:1024
	s_waitcnt vmcnt(15)
	v_mov_b32_e32 v1, v226
	v_mov_b32_e32 v24, v227
	v_mov_b32_e32 v25, v228
	v_mov_b32_e32 v16, v194
	v_mov_b32_e32 v17, v195
	v_mov_b32_e32 v18, v196
	v_mov_b32_e32 v19, v197
	v_mov_b32_e32 v14, v198
	v_mov_b32_e32 v15, v199
	v_mov_b32_e32 v12, v200
	v_mov_b32_e32 v13, v201
	v_mov_b32_e32 v20, v7
	v_mov_b32_e32 v21, v7
	v_bfe_u32 v47, v2, 3, 2
	v_alignbit_b32 v50, v3, v2, 5
	v_mad_u64_u32 v[52:53], s[16:17], v50, 48, s[4:5]
	v_lshlrev_b32_e32 v48, 2, v47
	v_lshl_add_u64 v[52:53], v[52:53], 0, v[48:49]
	v_lshlrev_b32_e32 v48, 6, v47
	global_load_dword v235, v[52:53], off
	global_load_dword v236, v[52:53], off offset:16
	global_load_dword v237, v[52:53], off offset:32
	v_mad_u64_u32 v[54:55], s[16:17], v50, s2, v[8:9]
	v_and_b32_e32 v224, 56, v4
	v_mov_b32_e32 v225, v49
	v_lshl_add_u64 v[52:53], v[54:55], 0, v[48:49]
	v_lshl_add_u64 v[52:53], v[52:53], 0, v[224:225]
	global_load_dwordx2 v[218:219], v[52:53], off nt
	global_load_dwordx2 v[220:221], v[52:53], off offset:256 nt
	global_load_dwordx2 v[222:223], v[52:53], off offset:512 nt
	v_mad_u64_u32 v[56:57], s[16:17], v50, s3, v[10:11]
	v_lshl_add_u64 v[56:57], v[56:57], 0, v[48:49]
	v_lshl_add_u64 v[224:225], v[56:57], 0, v[224:225]
	v_lshl_add_u64 v[2:3], v[2:3], 0, s[8:9]
	v_lshl_add_u64 v[4:5], v[4:5], 0, s[10:11]
	v_max3_f32 v6, v1, v24, v25
	v_sub_f32_e32 v1, v1, v6
	v_sub_f32_e32 v22, v24, v6
	v_sub_f32_e32 v6, v25, v6
	v_exp_f32_e32 v1, v1
	v_exp_f32_e32 v40, v22
	v_exp_f32_e32 v41, v6
	v_cvt_pk_f32_fp8_e32 v[26:27], v18
	v_cvt_pk_f32_fp8_e32 v[36:37], v19
	v_add_f32_e32 v6, v1, v40
	v_add_f32_e32 v6, v41, v6
	v_div_scale_f32 v42, s[16:17], v6, v6, 1.0
	v_rcp_f32_e32 v44, v42
	v_div_scale_f32 v43, vcc, 1.0, v6, 1.0
	v_cvt_pk_f32_fp8_e32 v[22:23], v16
	v_fma_f32 v45, -v42, v44, 1.0
	v_fmac_f32_e32 v44, v45, v44
	v_mul_f32_e32 v45, v43, v44
	v_fma_f32 v46, -v42, v45, v43
	v_fmac_f32_e32 v45, v46, v44
	v_fma_f32 v42, -v42, v45, v43
	v_cvt_pk_f32_fp8_sdwa v[28:29], v18 src0_sel:WORD_1
	v_cvt_pk_f32_fp8_e32 v[34:35], v17
	v_cvt_pk_f32_fp8_sdwa v[18:19], v19 src0_sel:WORD_1
	v_div_fmas_f32 v42, v42, v44, v45
	v_cvt_pk_f32_fp8_sdwa v[24:25], v16 src0_sel:WORD_1
	v_cvt_pk_f32_fp8_e32 v[30:31], v14
	v_cvt_pk_f32_fp8_sdwa v[16:17], v17 src0_sel:WORD_1
	v_cvt_pk_f32_fp8_e32 v[38:39], v15
	v_div_fixup_f32 v42, v42, v6, 1.0
	v_mul_f32_e32 v40, v40, v42
	v_mul_f32_e32 v6, v1, v42
	v_pk_mul_f32 v[26:27], v[26:27], v[40:41] op_sel_hi:[1,0]
	v_pk_mul_f32 v[36:37], v[40:41], v[36:37] op_sel_hi:[0,1]
	v_mul_f32_e32 v42, v41, v42
	v_pk_mul_f32 v[18:19], v[40:41], v[18:19] op_sel_hi:[0,1]
	v_pk_fma_f32 v[22:23], v[22:23], v[6:7], v[26:27] op_sel_hi:[1,0,1]
	v_pk_fma_f32 v[26:27], v[6:7], v[34:35], v[36:37] op_sel_hi:[0,1,1]
	v_cvt_pk_f32_fp8_sdwa v[32:33], v14 src0_sel:WORD_1
	v_cvt_pk_f32_fp8_sdwa v[14:15], v15 src0_sel:WORD_1
	v_pk_fma_f32 v[16:17], v[6:7], v[16:17], v[18:19] op_sel_hi:[0,1,1]
	v_pk_fma_f32 v[18:19], v[30:31], v[42:43], v[22:23] op_sel_hi:[1,0,1]
	v_pk_fma_f32 v[22:23], v[42:43], v[38:39], v[26:27] op_sel_hi:[0,1,1]
	v_cvt_pk_fp8_f32 v20, v18, v19
	v_cvt_pk_fp8_f32 v21, v22, v23
	v_pk_mul_f32 v[28:29], v[28:29], v[40:41] op_sel_hi:[1,0]
	v_pk_fma_f32 v[14:15], v[42:43], v[14:15], v[16:17] op_sel_hi:[0,1,1]
	v_pk_fma_f32 v[24:25], v[24:25], v[6:7], v[28:29] op_sel_hi:[1,0,1]
	v_cvt_pk_fp8_f32 v21, v14, v15 op_sel:[0,0,1]
	v_pk_fma_f32 v[18:19], v[32:33], v[42:43], v[24:25] op_sel_hi:[1,0,1]
	v_add_co_u32_e32 v12, vcc, 0xe000000, v12
	v_cvt_pk_fp8_f32 v20, v18, v19 op_sel:[0,0,1]
	s_nop 0
	v_addc_co_u32_e32 v13, vcc, 0, v13, vcc
	global_store_dwordx2 v[12:13], v[20:21], off offset:1024
	s_waitcnt vmcnt(15)
	v_mov_b32_e32 v1, v229
	v_mov_b32_e32 v24, v230
	v_mov_b32_e32 v25, v231
	v_mov_b32_e32 v16, v202
	v_mov_b32_e32 v17, v203
	v_mov_b32_e32 v18, v204
	v_mov_b32_e32 v19, v205
	v_mov_b32_e32 v14, v206
	v_mov_b32_e32 v15, v207
	v_mov_b32_e32 v12, v208
	v_mov_b32_e32 v13, v209
	v_mov_b32_e32 v20, v7
	v_mov_b32_e32 v21, v7
	v_bfe_u32 v47, v2, 3, 2
	v_alignbit_b32 v50, v3, v2, 5
	v_mad_u64_u32 v[52:53], s[16:17], v50, 48, s[4:5]
	v_lshlrev_b32_e32 v48, 2, v47
	v_lshl_add_u64 v[52:53], v[52:53], 0, v[48:49]
	v_lshlrev_b32_e32 v48, 6, v47
	global_load_dword v226, v[52:53], off
	global_load_dword v227, v[52:53], off offset:16
	global_load_dword v228, v[52:53], off offset:32
	v_mad_u64_u32 v[54:55], s[16:17], v50, s2, v[8:9]
	v_and_b32_e32 v200, 56, v4
	v_mov_b32_e32 v201, v49
	v_lshl_add_u64 v[52:53], v[54:55], 0, v[48:49]
	v_lshl_add_u64 v[52:53], v[52:53], 0, v[200:201]
	global_load_dwordx2 v[194:195], v[52:53], off nt
	global_load_dwordx2 v[196:197], v[52:53], off offset:256 nt
	global_load_dwordx2 v[198:199], v[52:53], off offset:512 nt
	v_mad_u64_u32 v[56:57], s[16:17], v50, s3, v[10:11]
	v_lshl_add_u64 v[56:57], v[56:57], 0, v[48:49]
	v_lshl_add_u64 v[200:201], v[56:57], 0, v[200:201]
	v_lshl_add_u64 v[2:3], v[2:3], 0, s[8:9]
	v_lshl_add_u64 v[4:5], v[4:5], 0, s[10:11]
	v_max3_f32 v6, v1, v24, v25
	v_sub_f32_e32 v1, v1, v6
	v_sub_f32_e32 v22, v24, v6
	v_sub_f32_e32 v6, v25, v6
	v_exp_f32_e32 v1, v1
	v_exp_f32_e32 v40, v22
	v_exp_f32_e32 v41, v6
	v_cvt_pk_f32_fp8_e32 v[26:27], v18
	v_cvt_pk_f32_fp8_e32 v[36:37], v19
	v_add_f32_e32 v6, v1, v40
	v_add_f32_e32 v6, v41, v6
	v_div_scale_f32 v42, s[16:17], v6, v6, 1.0
	v_rcp_f32_e32 v44, v42
	v_div_scale_f32 v43, vcc, 1.0, v6, 1.0
	v_cvt_pk_f32_fp8_e32 v[22:23], v16
	v_fma_f32 v45, -v42, v44, 1.0
	v_fmac_f32_e32 v44, v45, v44
	v_mul_f32_e32 v45, v43, v44
	v_fma_f32 v46, -v42, v45, v43
	v_fmac_f32_e32 v45, v46, v44
	v_fma_f32 v42, -v42, v45, v43
	v_cvt_pk_f32_fp8_sdwa v[28:29], v18 src0_sel:WORD_1
	v_cvt_pk_f32_fp8_e32 v[34:35], v17
	v_cvt_pk_f32_fp8_sdwa v[18:19], v19 src0_sel:WORD_1
	v_div_fmas_f32 v42, v42, v44, v45
	v_cvt_pk_f32_fp8_sdwa v[24:25], v16 src0_sel:WORD_1
	v_cvt_pk_f32_fp8_e32 v[30:31], v14
	v_cvt_pk_f32_fp8_sdwa v[16:17], v17 src0_sel:WORD_1
	v_cvt_pk_f32_fp8_e32 v[38:39], v15
	v_div_fixup_f32 v42, v42, v6, 1.0
	v_mul_f32_e32 v40, v40, v42
	v_mul_f32_e32 v6, v1, v42
	v_pk_mul_f32 v[26:27], v[26:27], v[40:41] op_sel_hi:[1,0]
	v_pk_mul_f32 v[36:37], v[40:41], v[36:37] op_sel_hi:[0,1]
	v_mul_f32_e32 v42, v41, v42
	v_pk_mul_f32 v[18:19], v[40:41], v[18:19] op_sel_hi:[0,1]
	v_pk_fma_f32 v[22:23], v[22:23], v[6:7], v[26:27] op_sel_hi:[1,0,1]
	v_pk_fma_f32 v[26:27], v[6:7], v[34:35], v[36:37] op_sel_hi:[0,1,1]
	v_cvt_pk_f32_fp8_sdwa v[32:33], v14 src0_sel:WORD_1
	v_cvt_pk_f32_fp8_sdwa v[14:15], v15 src0_sel:WORD_1
	v_pk_fma_f32 v[16:17], v[6:7], v[16:17], v[18:19] op_sel_hi:[0,1,1]
	v_pk_fma_f32 v[18:19], v[30:31], v[42:43], v[22:23] op_sel_hi:[1,0,1]
	v_pk_fma_f32 v[22:23], v[42:43], v[38:39], v[26:27] op_sel_hi:[0,1,1]
	v_cvt_pk_fp8_f32 v20, v18, v19
	v_cvt_pk_fp8_f32 v21, v22, v23
	v_pk_mul_f32 v[28:29], v[28:29], v[40:41] op_sel_hi:[1,0]
	v_pk_fma_f32 v[14:15], v[42:43], v[14:15], v[16:17] op_sel_hi:[0,1,1]
	v_pk_fma_f32 v[24:25], v[24:25], v[6:7], v[28:29] op_sel_hi:[1,0,1]
	v_cvt_pk_fp8_f32 v21, v14, v15 op_sel:[0,0,1]
	v_pk_fma_f32 v[18:19], v[32:33], v[42:43], v[24:25] op_sel_hi:[1,0,1]
	v_add_co_u32_e32 v12, vcc, 0xe000000, v12
	v_cvt_pk_fp8_f32 v20, v18, v19 op_sel:[0,0,1]
	s_nop 0
	v_addc_co_u32_e32 v13, vcc, 0, v13, vcc
	global_store_dwordx2 v[12:13], v[20:21], off offset:1024
	s_waitcnt vmcnt(15)
	v_mov_b32_e32 v1, v232
	v_mov_b32_e32 v24, v233
	v_mov_b32_e32 v25, v234
	v_mov_b32_e32 v16, v210
	v_mov_b32_e32 v17, v211
	v_mov_b32_e32 v18, v212
	v_mov_b32_e32 v19, v213
	v_mov_b32_e32 v14, v214
	v_mov_b32_e32 v15, v215
	v_mov_b32_e32 v12, v216
	v_mov_b32_e32 v13, v217
	v_mov_b32_e32 v20, v7
	v_mov_b32_e32 v21, v7
	v_bfe_u32 v47, v2, 3, 2
	v_alignbit_b32 v50, v3, v2, 5
	v_mad_u64_u32 v[52:53], s[16:17], v50, 48, s[4:5]
	v_lshlrev_b32_e32 v48, 2, v47
	v_lshl_add_u64 v[52:53], v[52:53], 0, v[48:49]
	v_lshlrev_b32_e32 v48, 6, v47
	global_load_dword v229, v[52:53], off
	global_load_dword v230, v[52:53], off offset:16
	global_load_dword v231, v[52:53], off offset:32
	v_mad_u64_u32 v[54:55], s[16:17], v50, s2, v[8:9]
	v_and_b32_e32 v208, 56, v4
	v_mov_b32_e32 v209, v49
	v_lshl_add_u64 v[52:53], v[54:55], 0, v[48:49]
	v_lshl_add_u64 v[52:53], v[52:53], 0, v[208:209]
	global_load_dwordx2 v[202:203], v[52:53], off nt
	global_load_dwordx2 v[204:205], v[52:53], off offset:256 nt
	global_load_dwordx2 v[206:207], v[52:53], off offset:512 nt
	v_mad_u64_u32 v[56:57], s[16:17], v50, s3, v[10:11]
	v_lshl_add_u64 v[56:57], v[56:57], 0, v[48:49]
	v_lshl_add_u64 v[208:209], v[56:57], 0, v[208:209]
	v_lshl_add_u64 v[2:3], v[2:3], 0, s[8:9]
	v_lshl_add_u64 v[4:5], v[4:5], 0, s[10:11]
	v_max3_f32 v6, v1, v24, v25
	v_sub_f32_e32 v1, v1, v6
	v_sub_f32_e32 v22, v24, v6
	v_sub_f32_e32 v6, v25, v6
	v_exp_f32_e32 v1, v1
	v_exp_f32_e32 v40, v22
	v_exp_f32_e32 v41, v6
	v_cvt_pk_f32_fp8_e32 v[26:27], v18
	v_cvt_pk_f32_fp8_e32 v[36:37], v19
	v_add_f32_e32 v6, v1, v40
	v_add_f32_e32 v6, v41, v6
	v_div_scale_f32 v42, s[16:17], v6, v6, 1.0
	v_rcp_f32_e32 v44, v42
	v_div_scale_f32 v43, vcc, 1.0, v6, 1.0
	v_cvt_pk_f32_fp8_e32 v[22:23], v16
	v_fma_f32 v45, -v42, v44, 1.0
	v_fmac_f32_e32 v44, v45, v44
	v_mul_f32_e32 v45, v43, v44
	v_fma_f32 v46, -v42, v45, v43
	v_fmac_f32_e32 v45, v46, v44
	v_fma_f32 v42, -v42, v45, v43
	v_cvt_pk_f32_fp8_sdwa v[28:29], v18 src0_sel:WORD_1
	v_cvt_pk_f32_fp8_e32 v[34:35], v17
	v_cvt_pk_f32_fp8_sdwa v[18:19], v19 src0_sel:WORD_1
	v_div_fmas_f32 v42, v42, v44, v45
	v_cvt_pk_f32_fp8_sdwa v[24:25], v16 src0_sel:WORD_1
	v_cvt_pk_f32_fp8_e32 v[30:31], v14
	v_cvt_pk_f32_fp8_sdwa v[16:17], v17 src0_sel:WORD_1
	v_cvt_pk_f32_fp8_e32 v[38:39], v15
	v_div_fixup_f32 v42, v42, v6, 1.0
	v_mul_f32_e32 v40, v40, v42
	v_mul_f32_e32 v6, v1, v42
	v_pk_mul_f32 v[26:27], v[26:27], v[40:41] op_sel_hi:[1,0]
	v_pk_mul_f32 v[36:37], v[40:41], v[36:37] op_sel_hi:[0,1]
	v_mul_f32_e32 v42, v41, v42
	v_pk_mul_f32 v[18:19], v[40:41], v[18:19] op_sel_hi:[0,1]
	v_pk_fma_f32 v[22:23], v[22:23], v[6:7], v[26:27] op_sel_hi:[1,0,1]
	v_pk_fma_f32 v[26:27], v[6:7], v[34:35], v[36:37] op_sel_hi:[0,1,1]
	v_cvt_pk_f32_fp8_sdwa v[32:33], v14 src0_sel:WORD_1
	v_cvt_pk_f32_fp8_sdwa v[14:15], v15 src0_sel:WORD_1
	v_pk_fma_f32 v[16:17], v[6:7], v[16:17], v[18:19] op_sel_hi:[0,1,1]
	v_pk_fma_f32 v[18:19], v[30:31], v[42:43], v[22:23] op_sel_hi:[1,0,1]
	v_pk_fma_f32 v[22:23], v[42:43], v[38:39], v[26:27] op_sel_hi:[0,1,1]
	v_cvt_pk_fp8_f32 v20, v18, v19
	v_cvt_pk_fp8_f32 v21, v22, v23
	v_pk_mul_f32 v[28:29], v[28:29], v[40:41] op_sel_hi:[1,0]
	v_pk_fma_f32 v[14:15], v[42:43], v[14:15], v[16:17] op_sel_hi:[0,1,1]
	v_pk_fma_f32 v[24:25], v[24:25], v[6:7], v[28:29] op_sel_hi:[1,0,1]
	v_cvt_pk_fp8_f32 v21, v14, v15 op_sel:[0,0,1]
	v_pk_fma_f32 v[18:19], v[32:33], v[42:43], v[24:25] op_sel_hi:[1,0,1]
	v_add_co_u32_e32 v12, vcc, 0xe000000, v12
	v_cvt_pk_fp8_f32 v20, v18, v19 op_sel:[0,0,1]
	s_nop 0
	v_addc_co_u32_e32 v13, vcc, 0, v13, vcc
	global_store_dwordx2 v[12:13], v[20:21], off offset:1024
	s_waitcnt vmcnt(15)
	v_mov_b32_e32 v1, v235
	v_mov_b32_e32 v24, v236
	v_mov_b32_e32 v25, v237
	v_mov_b32_e32 v16, v218
	v_mov_b32_e32 v17, v219
	v_mov_b32_e32 v18, v220
	v_mov_b32_e32 v19, v221
	v_mov_b32_e32 v14, v222
	v_mov_b32_e32 v15, v223
	v_mov_b32_e32 v12, v224
	v_mov_b32_e32 v13, v225
	v_mov_b32_e32 v20, v7
	v_mov_b32_e32 v21, v7
	v_bfe_u32 v47, v2, 3, 2
	v_alignbit_b32 v50, v3, v2, 5
	v_mad_u64_u32 v[52:53], s[16:17], v50, 48, s[4:5]
	v_lshlrev_b32_e32 v48, 2, v47
	v_lshl_add_u64 v[52:53], v[52:53], 0, v[48:49]
	v_lshlrev_b32_e32 v48, 6, v47
	global_load_dword v232, v[52:53], off
	global_load_dword v233, v[52:53], off offset:16
	global_load_dword v234, v[52:53], off offset:32
	v_mad_u64_u32 v[54:55], s[16:17], v50, s2, v[8:9]
	v_and_b32_e32 v216, 56, v4
	v_mov_b32_e32 v217, v49
	v_lshl_add_u64 v[52:53], v[54:55], 0, v[48:49]
	v_lshl_add_u64 v[52:53], v[52:53], 0, v[216:217]
	global_load_dwordx2 v[210:211], v[52:53], off nt
	global_load_dwordx2 v[212:213], v[52:53], off offset:256 nt
	global_load_dwordx2 v[214:215], v[52:53], off offset:512 nt
	v_mad_u64_u32 v[56:57], s[16:17], v50, s3, v[10:11]
	v_lshl_add_u64 v[56:57], v[56:57], 0, v[48:49]
	v_lshl_add_u64 v[216:217], v[56:57], 0, v[216:217]
	v_lshl_add_u64 v[2:3], v[2:3], 0, s[8:9]
	v_lshl_add_u64 v[4:5], v[4:5], 0, s[10:11]
	v_max3_f32 v6, v1, v24, v25
	v_sub_f32_e32 v1, v1, v6
	v_sub_f32_e32 v22, v24, v6
	v_sub_f32_e32 v6, v25, v6
	v_exp_f32_e32 v1, v1
	v_exp_f32_e32 v40, v22
	v_exp_f32_e32 v41, v6
	v_cvt_pk_f32_fp8_e32 v[26:27], v18
	v_cvt_pk_f32_fp8_e32 v[36:37], v19
	v_add_f32_e32 v6, v1, v40
	v_add_f32_e32 v6, v41, v6
	v_div_scale_f32 v42, s[16:17], v6, v6, 1.0
	v_rcp_f32_e32 v44, v42
	v_div_scale_f32 v43, vcc, 1.0, v6, 1.0
	v_cvt_pk_f32_fp8_e32 v[22:23], v16
	v_fma_f32 v45, -v42, v44, 1.0
	v_fmac_f32_e32 v44, v45, v44
	v_mul_f32_e32 v45, v43, v44
	v_fma_f32 v46, -v42, v45, v43
	v_fmac_f32_e32 v45, v46, v44
	v_fma_f32 v42, -v42, v45, v43
	v_cvt_pk_f32_fp8_sdwa v[28:29], v18 src0_sel:WORD_1
	v_cvt_pk_f32_fp8_e32 v[34:35], v17
	v_cvt_pk_f32_fp8_sdwa v[18:19], v19 src0_sel:WORD_1
	v_div_fmas_f32 v42, v42, v44, v45
	v_cvt_pk_f32_fp8_sdwa v[24:25], v16 src0_sel:WORD_1
	v_cvt_pk_f32_fp8_e32 v[30:31], v14
	v_cvt_pk_f32_fp8_sdwa v[16:17], v17 src0_sel:WORD_1
	v_cvt_pk_f32_fp8_e32 v[38:39], v15
	v_div_fixup_f32 v42, v42, v6, 1.0
	v_mul_f32_e32 v40, v40, v42
	v_mul_f32_e32 v6, v1, v42
	v_pk_mul_f32 v[26:27], v[26:27], v[40:41] op_sel_hi:[1,0]
	v_pk_mul_f32 v[36:37], v[40:41], v[36:37] op_sel_hi:[0,1]
	v_mul_f32_e32 v42, v41, v42
	v_pk_mul_f32 v[18:19], v[40:41], v[18:19] op_sel_hi:[0,1]
	v_pk_fma_f32 v[22:23], v[22:23], v[6:7], v[26:27] op_sel_hi:[1,0,1]
	v_pk_fma_f32 v[26:27], v[6:7], v[34:35], v[36:37] op_sel_hi:[0,1,1]
	v_cvt_pk_f32_fp8_sdwa v[32:33], v14 src0_sel:WORD_1
	v_cvt_pk_f32_fp8_sdwa v[14:15], v15 src0_sel:WORD_1
	v_pk_fma_f32 v[16:17], v[6:7], v[16:17], v[18:19] op_sel_hi:[0,1,1]
	v_pk_fma_f32 v[18:19], v[30:31], v[42:43], v[22:23] op_sel_hi:[1,0,1]
	v_pk_fma_f32 v[22:23], v[42:43], v[38:39], v[26:27] op_sel_hi:[0,1,1]
	v_cvt_pk_fp8_f32 v20, v18, v19
	v_cvt_pk_fp8_f32 v21, v22, v23
	v_pk_mul_f32 v[28:29], v[28:29], v[40:41] op_sel_hi:[1,0]
	v_pk_fma_f32 v[14:15], v[42:43], v[14:15], v[16:17] op_sel_hi:[0,1,1]
	v_pk_fma_f32 v[24:25], v[24:25], v[6:7], v[28:29] op_sel_hi:[1,0,1]
	v_cvt_pk_fp8_f32 v21, v14, v15 op_sel:[0,0,1]
	v_pk_fma_f32 v[18:19], v[32:33], v[42:43], v[24:25] op_sel_hi:[1,0,1]
	v_add_co_u32_e32 v12, vcc, 0xe000000, v12
	v_cvt_pk_fp8_f32 v20, v18, v19 op_sel:[0,0,1]
	s_nop 0
	v_addc_co_u32_e32 v13, vcc, 0, v13, vcc
	global_store_dwordx2 v[12:13], v[20:21], off offset:1024
	s_waitcnt vmcnt(15)
	v_mov_b32_e32 v1, v226
	v_mov_b32_e32 v24, v227
	v_mov_b32_e32 v25, v228
	v_mov_b32_e32 v16, v194
	v_mov_b32_e32 v17, v195
	v_mov_b32_e32 v18, v196
	v_mov_b32_e32 v19, v197
	v_mov_b32_e32 v14, v198
	v_mov_b32_e32 v15, v199
	v_mov_b32_e32 v12, v200
	v_mov_b32_e32 v13, v201
	v_mov_b32_e32 v20, v7
	v_mov_b32_e32 v21, v7
	v_bfe_u32 v47, v2, 3, 2
	v_alignbit_b32 v50, v3, v2, 5
	v_mad_u64_u32 v[52:53], s[16:17], v50, 48, s[4:5]
	v_lshlrev_b32_e32 v48, 2, v47
	v_lshl_add_u64 v[52:53], v[52:53], 0, v[48:49]
	v_lshlrev_b32_e32 v48, 6, v47
	global_load_dword v235, v[52:53], off
	global_load_dword v236, v[52:53], off offset:16
	global_load_dword v237, v[52:53], off offset:32
	v_mad_u64_u32 v[54:55], s[16:17], v50, s2, v[8:9]
	v_and_b32_e32 v224, 56, v4
	v_mov_b32_e32 v225, v49
	v_lshl_add_u64 v[52:53], v[54:55], 0, v[48:49]
	v_lshl_add_u64 v[52:53], v[52:53], 0, v[224:225]
	global_load_dwordx2 v[218:219], v[52:53], off nt
	global_load_dwordx2 v[220:221], v[52:53], off offset:256 nt
	global_load_dwordx2 v[222:223], v[52:53], off offset:512 nt
	v_mad_u64_u32 v[56:57], s[16:17], v50, s3, v[10:11]
	v_lshl_add_u64 v[56:57], v[56:57], 0, v[48:49]
	v_lshl_add_u64 v[224:225], v[56:57], 0, v[224:225]
	v_lshl_add_u64 v[2:3], v[2:3], 0, s[8:9]
	v_lshl_add_u64 v[4:5], v[4:5], 0, s[10:11]
	v_max3_f32 v6, v1, v24, v25
	v_sub_f32_e32 v1, v1, v6
	v_sub_f32_e32 v22, v24, v6
	v_sub_f32_e32 v6, v25, v6
	v_exp_f32_e32 v1, v1
	v_exp_f32_e32 v40, v22
	v_exp_f32_e32 v41, v6
	v_cvt_pk_f32_fp8_e32 v[26:27], v18
	v_cvt_pk_f32_fp8_e32 v[36:37], v19
	v_add_f32_e32 v6, v1, v40
	v_add_f32_e32 v6, v41, v6
	v_div_scale_f32 v42, s[16:17], v6, v6, 1.0
	v_rcp_f32_e32 v44, v42
	v_div_scale_f32 v43, vcc, 1.0, v6, 1.0
	v_cvt_pk_f32_fp8_e32 v[22:23], v16
	v_fma_f32 v45, -v42, v44, 1.0
	v_fmac_f32_e32 v44, v45, v44
	v_mul_f32_e32 v45, v43, v44
	v_fma_f32 v46, -v42, v45, v43
	v_fmac_f32_e32 v45, v46, v44
	v_fma_f32 v42, -v42, v45, v43
	v_cvt_pk_f32_fp8_sdwa v[28:29], v18 src0_sel:WORD_1
	v_cvt_pk_f32_fp8_e32 v[34:35], v17
	v_cvt_pk_f32_fp8_sdwa v[18:19], v19 src0_sel:WORD_1
	v_div_fmas_f32 v42, v42, v44, v45
	v_cvt_pk_f32_fp8_sdwa v[24:25], v16 src0_sel:WORD_1
	v_cvt_pk_f32_fp8_e32 v[30:31], v14
	v_cvt_pk_f32_fp8_sdwa v[16:17], v17 src0_sel:WORD_1
	v_cvt_pk_f32_fp8_e32 v[38:39], v15
	v_div_fixup_f32 v42, v42, v6, 1.0
	v_mul_f32_e32 v40, v40, v42
	v_mul_f32_e32 v6, v1, v42
	v_pk_mul_f32 v[26:27], v[26:27], v[40:41] op_sel_hi:[1,0]
	v_pk_mul_f32 v[36:37], v[40:41], v[36:37] op_sel_hi:[0,1]
	v_mul_f32_e32 v42, v41, v42
	v_pk_mul_f32 v[18:19], v[40:41], v[18:19] op_sel_hi:[0,1]
	v_pk_fma_f32 v[22:23], v[22:23], v[6:7], v[26:27] op_sel_hi:[1,0,1]
	v_pk_fma_f32 v[26:27], v[6:7], v[34:35], v[36:37] op_sel_hi:[0,1,1]
	v_cvt_pk_f32_fp8_sdwa v[32:33], v14 src0_sel:WORD_1
	v_cvt_pk_f32_fp8_sdwa v[14:15], v15 src0_sel:WORD_1
	v_pk_fma_f32 v[16:17], v[6:7], v[16:17], v[18:19] op_sel_hi:[0,1,1]
	v_pk_fma_f32 v[18:19], v[30:31], v[42:43], v[22:23] op_sel_hi:[1,0,1]
	v_pk_fma_f32 v[22:23], v[42:43], v[38:39], v[26:27] op_sel_hi:[0,1,1]
	v_cvt_pk_fp8_f32 v20, v18, v19
	v_cvt_pk_fp8_f32 v21, v22, v23
	v_pk_mul_f32 v[28:29], v[28:29], v[40:41] op_sel_hi:[1,0]
	v_pk_fma_f32 v[14:15], v[42:43], v[14:15], v[16:17] op_sel_hi:[0,1,1]
	v_pk_fma_f32 v[24:25], v[24:25], v[6:7], v[28:29] op_sel_hi:[1,0,1]
	v_cvt_pk_fp8_f32 v21, v14, v15 op_sel:[0,0,1]
	v_pk_fma_f32 v[18:19], v[32:33], v[42:43], v[24:25] op_sel_hi:[1,0,1]
	v_add_co_u32_e32 v12, vcc, 0xe000000, v12
	v_cvt_pk_fp8_f32 v20, v18, v19 op_sel:[0,0,1]
	s_nop 0
	v_addc_co_u32_e32 v13, vcc, 0, v13, vcc
	global_store_dwordx2 v[12:13], v[20:21], off offset:1024
	s_waitcnt vmcnt(15)
	v_mov_b32_e32 v1, v229
	v_mov_b32_e32 v24, v230
	v_mov_b32_e32 v25, v231
	v_mov_b32_e32 v16, v202
	v_mov_b32_e32 v17, v203
	v_mov_b32_e32 v18, v204
	v_mov_b32_e32 v19, v205
	v_mov_b32_e32 v14, v206
	v_mov_b32_e32 v15, v207
	v_mov_b32_e32 v12, v208
	v_mov_b32_e32 v13, v209
	v_mov_b32_e32 v20, v7
	v_mov_b32_e32 v21, v7
	v_max3_f32 v6, v1, v24, v25
	v_sub_f32_e32 v1, v1, v6
	v_sub_f32_e32 v22, v24, v6
	v_sub_f32_e32 v6, v25, v6
	v_exp_f32_e32 v1, v1
	v_exp_f32_e32 v40, v22
	v_exp_f32_e32 v41, v6
	v_cvt_pk_f32_fp8_e32 v[26:27], v18
	v_cvt_pk_f32_fp8_e32 v[36:37], v19
	v_add_f32_e32 v6, v1, v40
	v_add_f32_e32 v6, v41, v6
	v_div_scale_f32 v42, s[16:17], v6, v6, 1.0
	v_rcp_f32_e32 v44, v42
	v_div_scale_f32 v43, vcc, 1.0, v6, 1.0
	v_cvt_pk_f32_fp8_e32 v[22:23], v16
	v_fma_f32 v45, -v42, v44, 1.0
	v_fmac_f32_e32 v44, v45, v44
	v_mul_f32_e32 v45, v43, v44
	v_fma_f32 v46, -v42, v45, v43
	v_fmac_f32_e32 v45, v46, v44
	v_fma_f32 v42, -v42, v45, v43
	v_cvt_pk_f32_fp8_sdwa v[28:29], v18 src0_sel:WORD_1
	v_cvt_pk_f32_fp8_e32 v[34:35], v17
	v_cvt_pk_f32_fp8_sdwa v[18:19], v19 src0_sel:WORD_1
	v_div_fmas_f32 v42, v42, v44, v45
	v_cvt_pk_f32_fp8_sdwa v[24:25], v16 src0_sel:WORD_1
	v_cvt_pk_f32_fp8_e32 v[30:31], v14
	v_cvt_pk_f32_fp8_sdwa v[16:17], v17 src0_sel:WORD_1
	v_cvt_pk_f32_fp8_e32 v[38:39], v15
	v_div_fixup_f32 v42, v42, v6, 1.0
	v_mul_f32_e32 v40, v40, v42
	v_mul_f32_e32 v6, v1, v42
	v_pk_mul_f32 v[26:27], v[26:27], v[40:41] op_sel_hi:[1,0]
	v_pk_mul_f32 v[36:37], v[40:41], v[36:37] op_sel_hi:[0,1]
	v_mul_f32_e32 v42, v41, v42
	v_pk_mul_f32 v[18:19], v[40:41], v[18:19] op_sel_hi:[0,1]
	v_pk_fma_f32 v[22:23], v[22:23], v[6:7], v[26:27] op_sel_hi:[1,0,1]
	v_pk_fma_f32 v[26:27], v[6:7], v[34:35], v[36:37] op_sel_hi:[0,1,1]
	v_cvt_pk_f32_fp8_sdwa v[32:33], v14 src0_sel:WORD_1
	v_cvt_pk_f32_fp8_sdwa v[14:15], v15 src0_sel:WORD_1
	v_pk_fma_f32 v[16:17], v[6:7], v[16:17], v[18:19] op_sel_hi:[0,1,1]
	v_pk_fma_f32 v[18:19], v[30:31], v[42:43], v[22:23] op_sel_hi:[1,0,1]
	v_pk_fma_f32 v[22:23], v[42:43], v[38:39], v[26:27] op_sel_hi:[0,1,1]
	v_cvt_pk_fp8_f32 v20, v18, v19
	v_cvt_pk_fp8_f32 v21, v22, v23
	v_pk_mul_f32 v[28:29], v[28:29], v[40:41] op_sel_hi:[1,0]
	v_pk_fma_f32 v[14:15], v[42:43], v[14:15], v[16:17] op_sel_hi:[0,1,1]
	v_pk_fma_f32 v[24:25], v[24:25], v[6:7], v[28:29] op_sel_hi:[1,0,1]
	v_cvt_pk_fp8_f32 v21, v14, v15 op_sel:[0,0,1]
	v_pk_fma_f32 v[18:19], v[32:33], v[42:43], v[24:25] op_sel_hi:[1,0,1]
	v_add_co_u32_e32 v12, vcc, 0xe000000, v12
	v_cvt_pk_fp8_f32 v20, v18, v19 op_sel:[0,0,1]
	s_nop 0
	v_addc_co_u32_e32 v13, vcc, 0, v13, vcc
	global_store_dwordx2 v[12:13], v[20:21], off offset:1024
	s_waitcnt vmcnt(9)
	v_mov_b32_e32 v1, v232
	v_mov_b32_e32 v24, v233
	v_mov_b32_e32 v25, v234
	v_mov_b32_e32 v16, v210
	v_mov_b32_e32 v17, v211
	v_mov_b32_e32 v18, v212
	v_mov_b32_e32 v19, v213
	v_mov_b32_e32 v14, v214
	v_mov_b32_e32 v15, v215
	v_mov_b32_e32 v12, v216
	v_mov_b32_e32 v13, v217
	v_mov_b32_e32 v20, v7
	v_mov_b32_e32 v21, v7
	v_max3_f32 v6, v1, v24, v25
	v_sub_f32_e32 v1, v1, v6
	v_sub_f32_e32 v22, v24, v6
	v_sub_f32_e32 v6, v25, v6
	v_exp_f32_e32 v1, v1
	v_exp_f32_e32 v40, v22
	v_exp_f32_e32 v41, v6
	v_cvt_pk_f32_fp8_e32 v[26:27], v18
	v_cvt_pk_f32_fp8_e32 v[36:37], v19
	v_add_f32_e32 v6, v1, v40
	v_add_f32_e32 v6, v41, v6
	v_div_scale_f32 v42, s[16:17], v6, v6, 1.0
	v_rcp_f32_e32 v44, v42
	v_div_scale_f32 v43, vcc, 1.0, v6, 1.0
	v_cvt_pk_f32_fp8_e32 v[22:23], v16
	v_fma_f32 v45, -v42, v44, 1.0
	v_fmac_f32_e32 v44, v45, v44
	v_mul_f32_e32 v45, v43, v44
	v_fma_f32 v46, -v42, v45, v43
	v_fmac_f32_e32 v45, v46, v44
	v_fma_f32 v42, -v42, v45, v43
	v_cvt_pk_f32_fp8_sdwa v[28:29], v18 src0_sel:WORD_1
	v_cvt_pk_f32_fp8_e32 v[34:35], v17
	v_cvt_pk_f32_fp8_sdwa v[18:19], v19 src0_sel:WORD_1
	v_div_fmas_f32 v42, v42, v44, v45
	v_cvt_pk_f32_fp8_sdwa v[24:25], v16 src0_sel:WORD_1
	v_cvt_pk_f32_fp8_e32 v[30:31], v14
	v_cvt_pk_f32_fp8_sdwa v[16:17], v17 src0_sel:WORD_1
	v_cvt_pk_f32_fp8_e32 v[38:39], v15
	v_div_fixup_f32 v42, v42, v6, 1.0
	v_mul_f32_e32 v40, v40, v42
	v_mul_f32_e32 v6, v1, v42
	v_pk_mul_f32 v[26:27], v[26:27], v[40:41] op_sel_hi:[1,0]
	v_pk_mul_f32 v[36:37], v[40:41], v[36:37] op_sel_hi:[0,1]
	v_mul_f32_e32 v42, v41, v42
	v_pk_mul_f32 v[18:19], v[40:41], v[18:19] op_sel_hi:[0,1]
	v_pk_fma_f32 v[22:23], v[22:23], v[6:7], v[26:27] op_sel_hi:[1,0,1]
	v_pk_fma_f32 v[26:27], v[6:7], v[34:35], v[36:37] op_sel_hi:[0,1,1]
	v_cvt_pk_f32_fp8_sdwa v[32:33], v14 src0_sel:WORD_1
	v_cvt_pk_f32_fp8_sdwa v[14:15], v15 src0_sel:WORD_1
	v_pk_fma_f32 v[16:17], v[6:7], v[16:17], v[18:19] op_sel_hi:[0,1,1]
	v_pk_fma_f32 v[18:19], v[30:31], v[42:43], v[22:23] op_sel_hi:[1,0,1]
	v_pk_fma_f32 v[22:23], v[42:43], v[38:39], v[26:27] op_sel_hi:[0,1,1]
	v_cvt_pk_fp8_f32 v20, v18, v19
	v_cvt_pk_fp8_f32 v21, v22, v23
	v_pk_mul_f32 v[28:29], v[28:29], v[40:41] op_sel_hi:[1,0]
	v_pk_fma_f32 v[14:15], v[42:43], v[14:15], v[16:17] op_sel_hi:[0,1,1]
	v_pk_fma_f32 v[24:25], v[24:25], v[6:7], v[28:29] op_sel_hi:[1,0,1]
	v_cvt_pk_fp8_f32 v21, v14, v15 op_sel:[0,0,1]
	v_pk_fma_f32 v[18:19], v[32:33], v[42:43], v[24:25] op_sel_hi:[1,0,1]
	v_add_co_u32_e32 v12, vcc, 0xe000000, v12
	v_cvt_pk_fp8_f32 v20, v18, v19 op_sel:[0,0,1]
	s_nop 0
	v_addc_co_u32_e32 v13, vcc, 0, v13, vcc
	global_store_dwordx2 v[12:13], v[20:21], off offset:1024
	s_waitcnt vmcnt(3)
	v_mov_b32_e32 v1, v235
	v_mov_b32_e32 v24, v236
	v_mov_b32_e32 v25, v237
	v_mov_b32_e32 v16, v218
	v_mov_b32_e32 v17, v219
	v_mov_b32_e32 v18, v220
	v_mov_b32_e32 v19, v221
	v_mov_b32_e32 v14, v222
	v_mov_b32_e32 v15, v223
	v_mov_b32_e32 v12, v224
	v_mov_b32_e32 v13, v225
	v_mov_b32_e32 v20, v7
	v_mov_b32_e32 v21, v7
	v_max3_f32 v6, v1, v24, v25
	v_sub_f32_e32 v1, v1, v6
	v_sub_f32_e32 v22, v24, v6
	v_sub_f32_e32 v6, v25, v6
	v_exp_f32_e32 v1, v1
	v_exp_f32_e32 v40, v22
	v_exp_f32_e32 v41, v6
	v_cvt_pk_f32_fp8_e32 v[26:27], v18
	v_cvt_pk_f32_fp8_e32 v[36:37], v19
	v_add_f32_e32 v6, v1, v40
	v_add_f32_e32 v6, v41, v6
	v_div_scale_f32 v42, s[16:17], v6, v6, 1.0
	v_rcp_f32_e32 v44, v42
	v_div_scale_f32 v43, vcc, 1.0, v6, 1.0
	v_cvt_pk_f32_fp8_e32 v[22:23], v16
	v_fma_f32 v45, -v42, v44, 1.0
	v_fmac_f32_e32 v44, v45, v44
	v_mul_f32_e32 v45, v43, v44
	v_fma_f32 v46, -v42, v45, v43
	v_fmac_f32_e32 v45, v46, v44
	v_fma_f32 v42, -v42, v45, v43
	v_cvt_pk_f32_fp8_sdwa v[28:29], v18 src0_sel:WORD_1
	v_cvt_pk_f32_fp8_e32 v[34:35], v17
	v_cvt_pk_f32_fp8_sdwa v[18:19], v19 src0_sel:WORD_1
	v_div_fmas_f32 v42, v42, v44, v45
	v_cvt_pk_f32_fp8_sdwa v[24:25], v16 src0_sel:WORD_1
	v_cvt_pk_f32_fp8_e32 v[30:31], v14
	v_cvt_pk_f32_fp8_sdwa v[16:17], v17 src0_sel:WORD_1
	v_cvt_pk_f32_fp8_e32 v[38:39], v15
	v_div_fixup_f32 v42, v42, v6, 1.0
	v_mul_f32_e32 v40, v40, v42
	v_mul_f32_e32 v6, v1, v42
	v_pk_mul_f32 v[26:27], v[26:27], v[40:41] op_sel_hi:[1,0]
	v_pk_mul_f32 v[36:37], v[40:41], v[36:37] op_sel_hi:[0,1]
	v_mul_f32_e32 v42, v41, v42
	v_pk_mul_f32 v[18:19], v[40:41], v[18:19] op_sel_hi:[0,1]
	v_pk_fma_f32 v[22:23], v[22:23], v[6:7], v[26:27] op_sel_hi:[1,0,1]
	v_pk_fma_f32 v[26:27], v[6:7], v[34:35], v[36:37] op_sel_hi:[0,1,1]
	v_cvt_pk_f32_fp8_sdwa v[32:33], v14 src0_sel:WORD_1
	v_cvt_pk_f32_fp8_sdwa v[14:15], v15 src0_sel:WORD_1
	v_pk_fma_f32 v[16:17], v[6:7], v[16:17], v[18:19] op_sel_hi:[0,1,1]
	v_pk_fma_f32 v[18:19], v[30:31], v[42:43], v[22:23] op_sel_hi:[1,0,1]
	v_pk_fma_f32 v[22:23], v[42:43], v[38:39], v[26:27] op_sel_hi:[0,1,1]
	v_cvt_pk_fp8_f32 v20, v18, v19
	v_cvt_pk_fp8_f32 v21, v22, v23
	v_pk_mul_f32 v[28:29], v[28:29], v[40:41] op_sel_hi:[1,0]
	v_pk_fma_f32 v[14:15], v[42:43], v[14:15], v[16:17] op_sel_hi:[0,1,1]
	v_pk_fma_f32 v[24:25], v[24:25], v[6:7], v[28:29] op_sel_hi:[1,0,1]
	v_cvt_pk_fp8_f32 v21, v14, v15 op_sel:[0,0,1]
	v_pk_fma_f32 v[18:19], v[32:33], v[42:43], v[24:25] op_sel_hi:[1,0,1]
	v_add_co_u32_e32 v12, vcc, 0xe000000, v12
	v_cvt_pk_fp8_f32 v20, v18, v19 op_sel:[0,0,1]
	s_nop 0
	v_addc_co_u32_e32 v13, vcc, 0, v13, vcc
	global_store_dwordx2 v[12:13], v[20:21], off offset:1024
	s_branch .LBB0_409
